# back-edge rotation (loop-back barrier as loop head, counter/test/branch in front of it, exit-path barrier copy) on the six 8-phase GEMM K-loops
# baseline (speedup 1.0000x reference)
.LBB0_190:
	v_mov_b32_e32 v2, 0
	s_add_i32 s8, s67, 0xc0080
	s_add_i32 s9, s65, 0x100
	s_mov_b32 s65, -2
	v_mov_b32_e32 v3, v2
	v_mov_b32_e32 v4, v2
	v_mov_b32_e32 v5, v2
	v_mov_b32_e32 v6, v2
	v_mov_b32_e32 v7, v2
	v_mov_b32_e32 v8, v2
	v_mov_b32_e32 v9, v2
	v_mov_b32_e32 v10, v2
	v_mov_b32_e32 v11, v2
	v_mov_b32_e32 v12, v2
	v_mov_b32_e32 v13, v2
	v_mov_b32_e32 v18, v2
	v_mov_b32_e32 v19, v2
	v_mov_b32_e32 v20, v2
	v_mov_b32_e32 v21, v2
	v_mov_b32_e32 v26, v2
	v_mov_b32_e32 v27, v2
	v_mov_b32_e32 v28, v2
	v_mov_b32_e32 v29, v2
	v_mov_b32_e32 v34, v2
	v_mov_b32_e32 v35, v2
	v_mov_b32_e32 v36, v2
	v_mov_b32_e32 v37, v2
	v_mov_b32_e32 v42, v2
	v_mov_b32_e32 v43, v2
	v_mov_b32_e32 v44, v2
	v_mov_b32_e32 v45, v2
	v_mov_b32_e32 v50, v2
	v_mov_b32_e32 v51, v2
	v_mov_b32_e32 v52, v2
	v_mov_b32_e32 v53, v2
	v_mov_b32_e32 v14, v2
	v_mov_b32_e32 v15, v2
	v_mov_b32_e32 v16, v2
	v_mov_b32_e32 v17, v2
	v_mov_b32_e32 v22, v2
	v_mov_b32_e32 v23, v2
	v_mov_b32_e32 v24, v2
	v_mov_b32_e32 v25, v2
	v_mov_b32_e32 v30, v2
	v_mov_b32_e32 v31, v2
	v_mov_b32_e32 v32, v2
	v_mov_b32_e32 v33, v2
	v_mov_b32_e32 v38, v2
	v_mov_b32_e32 v39, v2
	v_mov_b32_e32 v40, v2
	v_mov_b32_e32 v41, v2
	v_mov_b32_e32 v46, v2
	v_mov_b32_e32 v47, v2
	v_mov_b32_e32 v48, v2
	v_mov_b32_e32 v49, v2
	v_mov_b32_e32 v54, v2
	v_mov_b32_e32 v55, v2
	v_mov_b32_e32 v56, v2
	v_mov_b32_e32 v57, v2
	v_mov_b32_e32 v58, v2
	v_mov_b32_e32 v59, v2
	v_mov_b32_e32 v60, v2
	v_mov_b32_e32 v61, v2
	v_mov_b32_e32 v62, v2
	v_mov_b32_e32 v63, v2
	v_mov_b32_e32 v64, v2
	v_mov_b32_e32 v65, v2
	v_mov_b32_e32 v66, v2
	v_mov_b32_e32 v67, v2
	v_mov_b32_e32 v68, v2
	v_mov_b32_e32 v69, v2
	v_mov_b32_e32 v70, v2
	v_mov_b32_e32 v71, v2
	v_mov_b32_e32 v72, v2
	v_mov_b32_e32 v73, v2
	v_mov_b32_e32 v74, v2
	v_mov_b32_e32 v75, v2
	v_mov_b32_e32 v76, v2
	v_mov_b32_e32 v77, v2
	v_mov_b32_e32 v82, v2
	v_mov_b32_e32 v83, v2
	v_mov_b32_e32 v84, v2
	v_mov_b32_e32 v85, v2
	v_mov_b32_e32 v90, v2
	v_mov_b32_e32 v91, v2
	v_mov_b32_e32 v92, v2
	v_mov_b32_e32 v93, v2
	v_mov_b32_e32 v98, v2
	v_mov_b32_e32 v99, v2
	v_mov_b32_e32 v100, v2
	v_mov_b32_e32 v101, v2
	v_mov_b32_e32 v106, v2
	v_mov_b32_e32 v107, v2
	v_mov_b32_e32 v108, v2
	v_mov_b32_e32 v109, v2
	v_mov_b32_e32 v114, v2
	v_mov_b32_e32 v115, v2
	v_mov_b32_e32 v116, v2
	v_mov_b32_e32 v117, v2
	v_mov_b32_e32 v78, v2
	v_mov_b32_e32 v79, v2
	v_mov_b32_e32 v80, v2
	v_mov_b32_e32 v81, v2
	v_mov_b32_e32 v86, v2
	v_mov_b32_e32 v87, v2
	v_mov_b32_e32 v88, v2
	v_mov_b32_e32 v89, v2
	v_mov_b32_e32 v94, v2
	v_mov_b32_e32 v95, v2
	v_mov_b32_e32 v96, v2
	v_mov_b32_e32 v97, v2
	v_mov_b32_e32 v102, v2
	v_mov_b32_e32 v103, v2
	v_mov_b32_e32 v104, v2
	v_mov_b32_e32 v105, v2
	v_mov_b32_e32 v110, v2
	v_mov_b32_e32 v111, v2
	v_mov_b32_e32 v112, v2
	v_mov_b32_e32 v113, v2
	v_mov_b32_e32 v118, v2
	v_mov_b32_e32 v119, v2
	v_mov_b32_e32 v120, v2
	v_mov_b32_e32 v121, v2
	v_mov_b32_e32 v122, v2
	v_mov_b32_e32 v123, v2
	v_mov_b32_e32 v124, v2
	v_mov_b32_e32 v125, v2
	v_mov_b32_e32 v126, v2
	v_mov_b32_e32 v127, v2
	v_mov_b32_e32 v128, v2
	v_mov_b32_e32 v129, v2
	s_branch .LBB0_191

.LBB0_191:
	ds_read_b128 v[134:137], v150
	ds_read_b128 v[156:159], v150 offset:1024
	ds_read_b128 v[160:163], v150 offset:2048
	ds_read_b128 v[164:167], v150 offset:3072
	ds_read_b128 v[168:171], v151
	ds_read_b128 v[172:175], v151 offset:1024
	ds_read_b128 v[176:179], v151 offset:2048
	ds_read_b128 v[180:183], v151 offset:3072
	s_add_i32 s67, s8, 0xfff40080
	s_cmp_eq_u32 s65, 28
	s_cselect_b32 s67, s63, s67
	s_cselect_b32 s69, s64, s9
	s_add_i32 s68, s67, 0x80
	s_add_i32 s70, s8, 0xfffc0000
	s_mov_b32 m0, s55
	ds_read_b128 v[184:187], v152
	ds_read_b128 v[188:191], v152 offset:1024
	ds_read_b128 v[192:195], v152 offset:2048
	ds_read_b128 v[196:199], v152 offset:3072
	ds_read_b128 v[200:203], v152 offset:4096
	ds_read_b128 v[204:207], v152 offset:5120
	ds_read_b128 v[208:211], v152 offset:6144
	ds_read_b128 v[212:215], v152 offset:7168
	buffer_load_dwordx4 v131, s[12:15], s70 offen lds
	s_mov_b32 m0, s56
	s_nop 0
	buffer_load_dwordx4 v131, s[12:15], s8 offen lds
	s_waitcnt vmcnt(8)
	s_waitcnt lgkmcnt(0)
	s_barrier
	s_setprio 1
	s_waitcnt lgkmcnt(7)
	v_mfma_f32_16x16x32_bf16 v[126:129], v[134:137], v[184:187], v[126:129]
	v_mfma_f32_16x16x32_bf16 v[122:125], v[160:163], v[184:187], v[122:125]
	s_waitcnt lgkmcnt(5)
	v_mfma_f32_16x16x32_bf16 v[118:121], v[134:137], v[192:195], v[118:121]
	v_mfma_f32_16x16x32_bf16 v[110:113], v[160:163], v[192:195], v[110:113]
	s_waitcnt lgkmcnt(3)
	v_mfma_f32_16x16x32_bf16 v[102:105], v[134:137], v[200:203], v[102:105]
	v_mfma_f32_16x16x32_bf16 v[94:97], v[160:163], v[200:203], v[94:97]
	s_waitcnt lgkmcnt(1)
	v_mfma_f32_16x16x32_bf16 v[86:89], v[134:137], v[208:211], v[86:89]
	v_mfma_f32_16x16x32_bf16 v[78:81], v[160:163], v[208:211], v[78:81]
	v_mfma_f32_16x16x32_bf16 v[126:129], v[156:159], v[188:191], v[126:129]
	v_mfma_f32_16x16x32_bf16 v[122:125], v[164:167], v[188:191], v[122:125]
	v_mfma_f32_16x16x32_bf16 v[118:121], v[156:159], v[196:199], v[118:121]
	v_mfma_f32_16x16x32_bf16 v[110:113], v[164:167], v[196:199], v[110:113]
	v_mfma_f32_16x16x32_bf16 v[102:105], v[156:159], v[204:207], v[102:105]
	v_mfma_f32_16x16x32_bf16 v[94:97], v[164:167], v[204:207], v[94:97]
	s_waitcnt lgkmcnt(0)
	v_mfma_f32_16x16x32_bf16 v[86:89], v[156:159], v[212:215], v[86:89]
	v_mfma_f32_16x16x32_bf16 v[78:81], v[164:167], v[212:215], v[78:81]
	s_setprio 0
	s_setprio 1
	v_mfma_f32_16x16x32_bf16 v[114:117], v[168:171], v[184:187], v[114:117]
	v_mfma_f32_16x16x32_bf16 v[106:109], v[176:179], v[184:187], v[106:109]
	v_mfma_f32_16x16x32_bf16 v[98:101], v[168:171], v[192:195], v[98:101]
	v_mfma_f32_16x16x32_bf16 v[90:93], v[176:179], v[192:195], v[90:93]
	v_mfma_f32_16x16x32_bf16 v[82:85], v[168:171], v[200:203], v[82:85]
	v_mfma_f32_16x16x32_bf16 v[74:77], v[176:179], v[200:203], v[74:77]
	v_mfma_f32_16x16x32_bf16 v[70:73], v[168:171], v[208:211], v[70:73]
	v_mfma_f32_16x16x32_bf16 v[66:69], v[176:179], v[208:211], v[66:69]
	v_mfma_f32_16x16x32_bf16 v[114:117], v[172:175], v[188:191], v[114:117]
	v_mfma_f32_16x16x32_bf16 v[106:109], v[180:183], v[188:191], v[106:109]
	v_mfma_f32_16x16x32_bf16 v[98:101], v[172:175], v[196:199], v[98:101]
	v_mfma_f32_16x16x32_bf16 v[90:93], v[180:183], v[196:199], v[90:93]
	v_mfma_f32_16x16x32_bf16 v[82:85], v[172:175], v[204:207], v[82:85]
	v_mfma_f32_16x16x32_bf16 v[74:77], v[180:183], v[204:207], v[74:77]
	v_mfma_f32_16x16x32_bf16 v[70:73], v[172:175], v[212:215], v[70:73]
	v_mfma_f32_16x16x32_bf16 v[66:69], v[180:183], v[212:215], v[66:69]
	s_setprio 0
	s_barrier
	s_mov_b32 m0, s29
	ds_read_b128 v[184:187], v152 offset:16384
	ds_read_b128 v[188:191], v152 offset:17408
	ds_read_b128 v[192:195], v152 offset:18432
	ds_read_b128 v[196:199], v152 offset:19456
	ds_read_b128 v[200:203], v152 offset:20480
	ds_read_b128 v[204:207], v152 offset:21504
	ds_read_b128 v[208:211], v152 offset:22528
	ds_read_b128 v[212:215], v152 offset:23552
	buffer_load_dwordx4 v148, s[12:15], s69 offen lds
	s_add_i32 s70, s69, 0x40000
	s_mov_b32 m0, s30
	s_nop 0
	buffer_load_dwordx4 v148, s[12:15], s70 offen lds
	s_add_i32 s70, s69, 0x80000
	s_mov_b32 m0, s31
	s_nop 0
	buffer_load_dwordx4 v148, s[12:15], s70 offen lds
	s_add_i32 s70, s69, 0xc0000
	s_mov_b32 m0, s34
	s_nop 0
	buffer_load_dwordx4 v148, s[12:15], s70 offen lds
	s_mov_b32 m0, s28
	s_add_i32 s70, s67, 0x40000
	buffer_load_dwordx4 v131, s[12:15], s67 offen lds
	s_mov_b32 m0, s35
	s_nop 0
	buffer_load_dwordx4 v131, s[12:15], s70 offen lds
	s_waitcnt vmcnt(8)
	s_waitcnt lgkmcnt(0)
	s_barrier
	s_setprio 1
	s_waitcnt lgkmcnt(7)
	v_mfma_f32_16x16x32_bf16 v[62:65], v[134:137], v[184:187], v[62:65]
	v_mfma_f32_16x16x32_bf16 v[58:61], v[160:163], v[184:187], v[58:61]
	s_waitcnt lgkmcnt(5)
	v_mfma_f32_16x16x32_bf16 v[54:57], v[134:137], v[192:195], v[54:57]
	v_mfma_f32_16x16x32_bf16 v[46:49], v[160:163], v[192:195], v[46:49]
	s_waitcnt lgkmcnt(3)
	v_mfma_f32_16x16x32_bf16 v[38:41], v[134:137], v[200:203], v[38:41]
	v_mfma_f32_16x16x32_bf16 v[30:33], v[160:163], v[200:203], v[30:33]
	s_waitcnt lgkmcnt(1)
	v_mfma_f32_16x16x32_bf16 v[22:25], v[134:137], v[208:211], v[22:25]
	v_mfma_f32_16x16x32_bf16 v[14:17], v[160:163], v[208:211], v[14:17]
	v_mfma_f32_16x16x32_bf16 v[62:65], v[156:159], v[188:191], v[62:65]
	v_mfma_f32_16x16x32_bf16 v[58:61], v[164:167], v[188:191], v[58:61]
	v_mfma_f32_16x16x32_bf16 v[54:57], v[156:159], v[196:199], v[54:57]
	v_mfma_f32_16x16x32_bf16 v[46:49], v[164:167], v[196:199], v[46:49]
	v_mfma_f32_16x16x32_bf16 v[38:41], v[156:159], v[204:207], v[38:41]
	v_mfma_f32_16x16x32_bf16 v[30:33], v[164:167], v[204:207], v[30:33]
	s_waitcnt lgkmcnt(0)
	v_mfma_f32_16x16x32_bf16 v[22:25], v[156:159], v[212:215], v[22:25]
	v_mfma_f32_16x16x32_bf16 v[14:17], v[164:167], v[212:215], v[14:17]
	s_setprio 0
	s_setprio 1
	v_mfma_f32_16x16x32_bf16 v[50:53], v[168:171], v[184:187], v[50:53]
	v_mfma_f32_16x16x32_bf16 v[42:45], v[176:179], v[184:187], v[42:45]
	v_mfma_f32_16x16x32_bf16 v[34:37], v[168:171], v[192:195], v[34:37]
	v_mfma_f32_16x16x32_bf16 v[26:29], v[176:179], v[192:195], v[26:29]
	v_mfma_f32_16x16x32_bf16 v[18:21], v[168:171], v[200:203], v[18:21]
	v_mfma_f32_16x16x32_bf16 v[10:13], v[176:179], v[200:203], v[10:13]
	v_mfma_f32_16x16x32_bf16 v[6:9], v[168:171], v[208:211], v[6:9]
	v_mfma_f32_16x16x32_bf16 v[2:5], v[176:179], v[208:211], v[2:5]
	v_mfma_f32_16x16x32_bf16 v[50:53], v[172:175], v[188:191], v[50:53]
	v_mfma_f32_16x16x32_bf16 v[42:45], v[180:183], v[188:191], v[42:45]
	v_mfma_f32_16x16x32_bf16 v[34:37], v[172:175], v[196:199], v[34:37]
	v_mfma_f32_16x16x32_bf16 v[26:29], v[180:183], v[196:199], v[26:29]
	v_mfma_f32_16x16x32_bf16 v[18:21], v[172:175], v[204:207], v[18:21]
	v_mfma_f32_16x16x32_bf16 v[10:13], v[180:183], v[204:207], v[10:13]
	v_mfma_f32_16x16x32_bf16 v[6:9], v[172:175], v[212:215], v[6:9]
	v_mfma_f32_16x16x32_bf16 v[2:5], v[180:183], v[212:215], v[2:5]
	s_setprio 0
	s_barrier
	ds_read_b128 v[134:137], v153
	ds_read_b128 v[156:159], v153 offset:1024
	ds_read_b128 v[160:163], v153 offset:2048
	ds_read_b128 v[164:167], v153 offset:3072
	ds_read_b128 v[168:171], v154
	ds_read_b128 v[172:175], v154 offset:1024
	ds_read_b128 v[176:179], v154 offset:2048
	ds_read_b128 v[180:183], v154 offset:3072
	s_mov_b32 m0, s36
	s_add_i32 s70, s67, 0x80000
	ds_read_b128 v[184:187], v152 offset:32768
	ds_read_b128 v[188:191], v152 offset:33792
	ds_read_b128 v[192:195], v152 offset:34816
	ds_read_b128 v[196:199], v152 offset:35840
	ds_read_b128 v[200:203], v152 offset:36864
	ds_read_b128 v[204:207], v152 offset:37888
	ds_read_b128 v[208:211], v152 offset:38912
	ds_read_b128 v[212:215], v152 offset:39936
	buffer_load_dwordx4 v131, s[12:15], s70 offen lds
	s_add_i32 s70, s67, 0xc0000
	s_mov_b32 m0, s37
	s_nop 0
	buffer_load_dwordx4 v131, s[12:15], s70 offen lds
	s_waitcnt vmcnt(8)
	s_waitcnt lgkmcnt(0)
	s_barrier
	s_setprio 1
	s_waitcnt lgkmcnt(7)
	v_mfma_f32_16x16x32_bf16 v[126:129], v[134:137], v[184:187], v[126:129]
	v_mfma_f32_16x16x32_bf16 v[122:125], v[160:163], v[184:187], v[122:125]
	s_waitcnt lgkmcnt(5)
	v_mfma_f32_16x16x32_bf16 v[118:121], v[134:137], v[192:195], v[118:121]
	v_mfma_f32_16x16x32_bf16 v[110:113], v[160:163], v[192:195], v[110:113]
	s_waitcnt lgkmcnt(3)
	v_mfma_f32_16x16x32_bf16 v[102:105], v[134:137], v[200:203], v[102:105]
	v_mfma_f32_16x16x32_bf16 v[94:97], v[160:163], v[200:203], v[94:97]
	s_waitcnt lgkmcnt(1)
	v_mfma_f32_16x16x32_bf16 v[86:89], v[134:137], v[208:211], v[86:89]
	v_mfma_f32_16x16x32_bf16 v[78:81], v[160:163], v[208:211], v[78:81]
	v_mfma_f32_16x16x32_bf16 v[126:129], v[156:159], v[188:191], v[126:129]
	v_mfma_f32_16x16x32_bf16 v[122:125], v[164:167], v[188:191], v[122:125]
	v_mfma_f32_16x16x32_bf16 v[118:121], v[156:159], v[196:199], v[118:121]
	v_mfma_f32_16x16x32_bf16 v[110:113], v[164:167], v[196:199], v[110:113]
	v_mfma_f32_16x16x32_bf16 v[102:105], v[156:159], v[204:207], v[102:105]
	v_mfma_f32_16x16x32_bf16 v[94:97], v[164:167], v[204:207], v[94:97]
	s_waitcnt lgkmcnt(0)
	v_mfma_f32_16x16x32_bf16 v[86:89], v[156:159], v[212:215], v[86:89]
	v_mfma_f32_16x16x32_bf16 v[78:81], v[164:167], v[212:215], v[78:81]
	s_setprio 0
	s_setprio 1
	v_mfma_f32_16x16x32_bf16 v[114:117], v[168:171], v[184:187], v[114:117]
	v_mfma_f32_16x16x32_bf16 v[106:109], v[176:179], v[184:187], v[106:109]
	v_mfma_f32_16x16x32_bf16 v[98:101], v[168:171], v[192:195], v[98:101]
	v_mfma_f32_16x16x32_bf16 v[90:93], v[176:179], v[192:195], v[90:93]
	v_mfma_f32_16x16x32_bf16 v[82:85], v[168:171], v[200:203], v[82:85]
	v_mfma_f32_16x16x32_bf16 v[74:77], v[176:179], v[200:203], v[74:77]
	v_mfma_f32_16x16x32_bf16 v[70:73], v[168:171], v[208:211], v[70:73]
	v_mfma_f32_16x16x32_bf16 v[66:69], v[176:179], v[208:211], v[66:69]
	v_mfma_f32_16x16x32_bf16 v[114:117], v[172:175], v[188:191], v[114:117]
	v_mfma_f32_16x16x32_bf16 v[106:109], v[180:183], v[188:191], v[106:109]
	v_mfma_f32_16x16x32_bf16 v[98:101], v[172:175], v[196:199], v[98:101]
	v_mfma_f32_16x16x32_bf16 v[90:93], v[180:183], v[196:199], v[90:93]
	v_mfma_f32_16x16x32_bf16 v[82:85], v[172:175], v[204:207], v[82:85]
	v_mfma_f32_16x16x32_bf16 v[74:77], v[180:183], v[204:207], v[74:77]
	v_mfma_f32_16x16x32_bf16 v[70:73], v[172:175], v[212:215], v[70:73]
	v_mfma_f32_16x16x32_bf16 v[66:69], v[180:183], v[212:215], v[66:69]
	s_setprio 0
	s_barrier
	s_mov_b32 m0, s39
	s_add_i32 s70, s69, 0x80
	ds_read_b128 v[184:187], v152 offset:49152
	ds_read_b128 v[188:191], v152 offset:50176
	ds_read_b128 v[192:195], v152 offset:51200
	ds_read_b128 v[196:199], v152 offset:52224
	ds_read_b128 v[200:203], v152 offset:53248
	ds_read_b128 v[204:207], v152 offset:54272
	ds_read_b128 v[208:211], v152 offset:55296
	ds_read_b128 v[212:215], v152 offset:56320
	buffer_load_dwordx4 v148, s[12:15], s70 offen lds
	s_add_i32 s70, s69, 0x40080
	s_mov_b32 m0, s40
	s_add_i32 s67, s67, 0x40080
	buffer_load_dwordx4 v148, s[12:15], s70 offen lds
	s_add_i32 s70, s69, 0x80080
	s_mov_b32 m0, s43
	s_add_i32 s69, s69, 0xc0080
	buffer_load_dwordx4 v148, s[12:15], s70 offen lds
	s_mov_b32 m0, s49
	s_nop 0
	buffer_load_dwordx4 v148, s[12:15], s69 offen lds
	s_mov_b32 m0, s41
	s_nop 0
	buffer_load_dwordx4 v131, s[12:15], s68 offen lds
	s_mov_b32 m0, s42
	s_nop 0
	buffer_load_dwordx4 v131, s[12:15], s67 offen lds
	s_waitcnt vmcnt(8)
	s_waitcnt lgkmcnt(0)
	s_barrier
	s_setprio 1
	s_waitcnt lgkmcnt(7)
	v_mfma_f32_16x16x32_bf16 v[62:65], v[134:137], v[184:187], v[62:65]
	v_mfma_f32_16x16x32_bf16 v[58:61], v[160:163], v[184:187], v[58:61]
	s_waitcnt lgkmcnt(5)
	v_mfma_f32_16x16x32_bf16 v[54:57], v[134:137], v[192:195], v[54:57]
	v_mfma_f32_16x16x32_bf16 v[46:49], v[160:163], v[192:195], v[46:49]
	s_waitcnt lgkmcnt(3)
	v_mfma_f32_16x16x32_bf16 v[38:41], v[134:137], v[200:203], v[38:41]
	v_mfma_f32_16x16x32_bf16 v[30:33], v[160:163], v[200:203], v[30:33]
	s_waitcnt lgkmcnt(1)
	v_mfma_f32_16x16x32_bf16 v[22:25], v[134:137], v[208:211], v[22:25]
	v_mfma_f32_16x16x32_bf16 v[14:17], v[160:163], v[208:211], v[14:17]
	v_mfma_f32_16x16x32_bf16 v[62:65], v[156:159], v[188:191], v[62:65]
	v_mfma_f32_16x16x32_bf16 v[58:61], v[164:167], v[188:191], v[58:61]
	v_mfma_f32_16x16x32_bf16 v[54:57], v[156:159], v[196:199], v[54:57]
	v_mfma_f32_16x16x32_bf16 v[46:49], v[164:167], v[196:199], v[46:49]
	v_mfma_f32_16x16x32_bf16 v[38:41], v[156:159], v[204:207], v[38:41]
	v_mfma_f32_16x16x32_bf16 v[30:33], v[164:167], v[204:207], v[30:33]
	s_waitcnt lgkmcnt(0)
	v_mfma_f32_16x16x32_bf16 v[22:25], v[156:159], v[212:215], v[22:25]
	v_mfma_f32_16x16x32_bf16 v[14:17], v[164:167], v[212:215], v[14:17]
	s_setprio 0
	s_setprio 1
	v_mfma_f32_16x16x32_bf16 v[50:53], v[168:171], v[184:187], v[50:53]
	v_mfma_f32_16x16x32_bf16 v[42:45], v[176:179], v[184:187], v[42:45]
	v_mfma_f32_16x16x32_bf16 v[34:37], v[168:171], v[192:195], v[34:37]
	v_mfma_f32_16x16x32_bf16 v[26:29], v[176:179], v[192:195], v[26:29]
	v_mfma_f32_16x16x32_bf16 v[18:21], v[168:171], v[200:203], v[18:21]
	v_mfma_f32_16x16x32_bf16 v[10:13], v[176:179], v[200:203], v[10:13]
	v_mfma_f32_16x16x32_bf16 v[6:9], v[168:171], v[208:211], v[6:9]
	v_mfma_f32_16x16x32_bf16 v[2:5], v[176:179], v[208:211], v[2:5]
	v_mfma_f32_16x16x32_bf16 v[50:53], v[172:175], v[188:191], v[50:53]
	v_mfma_f32_16x16x32_bf16 v[42:45], v[180:183], v[188:191], v[42:45]
	v_mfma_f32_16x16x32_bf16 v[34:37], v[172:175], v[196:199], v[34:37]
	v_mfma_f32_16x16x32_bf16 v[26:29], v[180:183], v[196:199], v[26:29]
	v_mfma_f32_16x16x32_bf16 v[18:21], v[172:175], v[204:207], v[18:21]
	v_mfma_f32_16x16x32_bf16 v[10:13], v[180:183], v[204:207], v[10:13]
	v_mfma_f32_16x16x32_bf16 v[6:9], v[172:175], v[212:215], v[6:9]
	v_mfma_f32_16x16x32_bf16 v[2:5], v[180:183], v[212:215], v[2:5]
	s_setprio 0
	s_add_i32 s65, s65, 2
	s_addk_i32 s8, 0x100
	s_addk_i32 s9, 0x100
	s_cmp_gt_u32 s65, 29
	s_cbranch_scc0 .Lkbar5
	s_barrier
	s_and_b64 vcc, exec, s[22:23]
	s_cbranch_vccz .LBB0_194
	s_barrier

.LBB0_260:
	v_mov_b32_e32 v2, 0
	s_add_i32 s34, s76, 0x60080
	s_add_i32 s35, s75, 0x100
	s_mov_b32 s75, -2
	v_mov_b32_e32 v3, v2
	v_mov_b32_e32 v4, v2
	v_mov_b32_e32 v5, v2
	v_mov_b32_e32 v6, v2
	v_mov_b32_e32 v7, v2
	v_mov_b32_e32 v8, v2
	v_mov_b32_e32 v9, v2
	v_mov_b32_e32 v10, v2
	v_mov_b32_e32 v11, v2
	v_mov_b32_e32 v12, v2
	v_mov_b32_e32 v13, v2
	v_mov_b32_e32 v14, v2
	v_mov_b32_e32 v15, v2
	v_mov_b32_e32 v16, v2
	v_mov_b32_e32 v17, v2
	v_mov_b32_e32 v26, v2
	v_mov_b32_e32 v27, v2
	v_mov_b32_e32 v28, v2
	v_mov_b32_e32 v29, v2
	v_mov_b32_e32 v30, v2
	v_mov_b32_e32 v31, v2
	v_mov_b32_e32 v32, v2
	v_mov_b32_e32 v33, v2
	v_mov_b32_e32 v42, v2
	v_mov_b32_e32 v43, v2
	v_mov_b32_e32 v44, v2
	v_mov_b32_e32 v45, v2
	v_mov_b32_e32 v46, v2
	v_mov_b32_e32 v47, v2
	v_mov_b32_e32 v48, v2
	v_mov_b32_e32 v49, v2
	v_mov_b32_e32 v18, v2
	v_mov_b32_e32 v19, v2
	v_mov_b32_e32 v20, v2
	v_mov_b32_e32 v21, v2
	v_mov_b32_e32 v22, v2
	v_mov_b32_e32 v23, v2
	v_mov_b32_e32 v24, v2
	v_mov_b32_e32 v25, v2
	v_mov_b32_e32 v34, v2
	v_mov_b32_e32 v35, v2
	v_mov_b32_e32 v36, v2
	v_mov_b32_e32 v37, v2
	v_mov_b32_e32 v38, v2
	v_mov_b32_e32 v39, v2
	v_mov_b32_e32 v40, v2
	v_mov_b32_e32 v41, v2
	v_mov_b32_e32 v50, v2
	v_mov_b32_e32 v51, v2
	v_mov_b32_e32 v52, v2
	v_mov_b32_e32 v53, v2
	v_mov_b32_e32 v54, v2
	v_mov_b32_e32 v55, v2
	v_mov_b32_e32 v56, v2
	v_mov_b32_e32 v57, v2
	v_mov_b32_e32 v58, v2
	v_mov_b32_e32 v59, v2
	v_mov_b32_e32 v60, v2
	v_mov_b32_e32 v61, v2
	v_mov_b32_e32 v62, v2
	v_mov_b32_e32 v63, v2
	v_mov_b32_e32 v64, v2
	v_mov_b32_e32 v65, v2
	v_mov_b32_e32 v66, v2
	v_mov_b32_e32 v67, v2
	v_mov_b32_e32 v68, v2
	v_mov_b32_e32 v69, v2
	v_mov_b32_e32 v70, v2
	v_mov_b32_e32 v71, v2
	v_mov_b32_e32 v72, v2
	v_mov_b32_e32 v73, v2
	v_mov_b32_e32 v74, v2
	v_mov_b32_e32 v75, v2
	v_mov_b32_e32 v76, v2
	v_mov_b32_e32 v77, v2
	v_mov_b32_e32 v78, v2
	v_mov_b32_e32 v79, v2
	v_mov_b32_e32 v80, v2
	v_mov_b32_e32 v81, v2
	v_mov_b32_e32 v90, v2
	v_mov_b32_e32 v91, v2
	v_mov_b32_e32 v92, v2
	v_mov_b32_e32 v93, v2
	v_mov_b32_e32 v94, v2
	v_mov_b32_e32 v95, v2
	v_mov_b32_e32 v96, v2
	v_mov_b32_e32 v97, v2
	v_mov_b32_e32 v106, v2
	v_mov_b32_e32 v107, v2
	v_mov_b32_e32 v108, v2
	v_mov_b32_e32 v109, v2
	v_mov_b32_e32 v110, v2
	v_mov_b32_e32 v111, v2
	v_mov_b32_e32 v112, v2
	v_mov_b32_e32 v113, v2
	v_mov_b32_e32 v82, v2
	v_mov_b32_e32 v83, v2
	v_mov_b32_e32 v84, v2
	v_mov_b32_e32 v85, v2
	v_mov_b32_e32 v86, v2
	v_mov_b32_e32 v87, v2
	v_mov_b32_e32 v88, v2
	v_mov_b32_e32 v89, v2
	v_mov_b32_e32 v98, v2
	v_mov_b32_e32 v99, v2
	v_mov_b32_e32 v100, v2
	v_mov_b32_e32 v101, v2
	v_mov_b32_e32 v102, v2
	v_mov_b32_e32 v103, v2
	v_mov_b32_e32 v104, v2
	v_mov_b32_e32 v105, v2
	v_mov_b32_e32 v114, v2
	v_mov_b32_e32 v115, v2
	v_mov_b32_e32 v116, v2
	v_mov_b32_e32 v117, v2
	v_mov_b32_e32 v118, v2
	v_mov_b32_e32 v119, v2
	v_mov_b32_e32 v120, v2
	v_mov_b32_e32 v121, v2
	v_mov_b32_e32 v122, v2
	v_mov_b32_e32 v123, v2
	v_mov_b32_e32 v124, v2
	v_mov_b32_e32 v125, v2
	v_mov_b32_e32 v126, v2
	v_mov_b32_e32 v127, v2
	v_mov_b32_e32 v128, v2
	v_mov_b32_e32 v129, v2
	s_branch .LBB0_261

.LBB0_261:
	ds_read_b128 v[132:135], v144
	ds_read_b128 v[136:139], v144 offset:1024
	ds_read_b128 v[152:155], v144 offset:2048
	ds_read_b128 v[156:159], v144 offset:3072
	ds_read_b128 v[160:163], v145
	ds_read_b128 v[164:167], v145 offset:1024
	ds_read_b128 v[168:171], v145 offset:2048
	ds_read_b128 v[172:175], v145 offset:3072
	s_add_i32 s12, s34, 0xfffa0080
	s_cmp_eq_u32 s75, 12
	s_cselect_b32 s76, s72, s12
	s_cselect_b32 s78, s73, s35
	s_add_i32 s77, s76, 0x80
	s_add_i32 s79, s34, 0xfffe0000
	s_mov_b32 s12, s44
	s_mov_b32 m0, s58
	ds_read_b128 v[176:179], v146
	ds_read_b128 v[180:183], v146 offset:1024
	ds_read_b128 v[184:187], v146 offset:2048
	ds_read_b128 v[188:191], v146 offset:3072
	ds_read_b128 v[192:195], v146 offset:4096
	ds_read_b128 v[196:199], v146 offset:5120
	ds_read_b128 v[200:203], v146 offset:6144
	ds_read_b128 v[204:207], v146 offset:7168
	buffer_load_dwordx4 v142, s[12:15], s79 offen lds
	s_mov_b32 m0, s59
	s_nop 0
	buffer_load_dwordx4 v142, s[12:15], s34 offen lds
	s_waitcnt vmcnt(8)
	s_waitcnt lgkmcnt(0)
	s_barrier
	s_setprio 1
	s_waitcnt lgkmcnt(6)
	v_mfma_scale_f32_16x16x128_f8f6f4 v[126:129], v[132:139], v[176:183], v[126:129], v148, v147 op_sel_hi:[0,0,0]
	v_mfma_scale_f32_16x16x128_f8f6f4 v[122:125], v[152:159], v[176:183], v[122:125], v148, v147 op_sel_hi:[0,0,0]
	s_waitcnt lgkmcnt(4)
	v_mfma_scale_f32_16x16x128_f8f6f4 v[118:121], v[132:139], v[184:191], v[118:121], v148, v147 op_sel_hi:[0,0,0]
	v_mfma_scale_f32_16x16x128_f8f6f4 v[114:117], v[152:159], v[184:191], v[114:117], v148, v147 op_sel_hi:[0,0,0]
	s_waitcnt lgkmcnt(2)
	v_mfma_scale_f32_16x16x128_f8f6f4 v[102:105], v[132:139], v[192:199], v[102:105], v148, v147 op_sel_hi:[0,0,0]
	v_mfma_scale_f32_16x16x128_f8f6f4 v[98:101], v[152:159], v[192:199], v[98:101], v148, v147 op_sel_hi:[0,0,0]
	s_waitcnt lgkmcnt(0)
	v_mfma_scale_f32_16x16x128_f8f6f4 v[208:211], v[132:139], v[200:207], v[86:89], v148, v147 op_sel_hi:[0,0,0]
	v_mfma_scale_f32_16x16x128_f8f6f4 v[212:215], v[152:159], v[200:207], v[82:85], v148, v147 op_sel_hi:[0,0,0]
	s_setprio 0
	s_setprio 1
	v_mfma_scale_f32_16x16x128_f8f6f4 v[110:113], v[160:167], v[176:183], v[110:113], v148, v147 op_sel_hi:[0,0,0]
	v_mfma_scale_f32_16x16x128_f8f6f4 v[106:109], v[168:175], v[176:183], v[106:109], v148, v147 op_sel_hi:[0,0,0]
	v_mfma_scale_f32_16x16x128_f8f6f4 v[176:179], v[160:167], v[184:191], v[94:97], v148, v147 op_sel_hi:[0,0,0]
	v_mfma_scale_f32_16x16x128_f8f6f4 v[180:183], v[168:175], v[184:191], v[90:93], v148, v147 op_sel_hi:[0,0,0]
	v_mfma_scale_f32_16x16x128_f8f6f4 v[184:187], v[160:167], v[192:199], v[78:81], v148, v147 op_sel_hi:[0,0,0]
	v_mfma_scale_f32_16x16x128_f8f6f4 v[188:191], v[168:175], v[192:199], v[74:77], v148, v147 op_sel_hi:[0,0,0]
	v_mfma_scale_f32_16x16x128_f8f6f4 v[192:195], v[160:167], v[200:207], v[70:73], v148, v147 op_sel_hi:[0,0,0]
	v_mfma_scale_f32_16x16x128_f8f6f4 v[196:199], v[168:175], v[200:207], v[66:69], v148, v147 op_sel_hi:[0,0,0]
	s_setprio 0
	s_barrier
	s_mov_b32 m0, s23
	s_nop 3
	ds_read_b128 v[66:69], v146 offset:16384
	ds_read_b128 v[70:73], v146 offset:17408
	ds_read_b128 v[74:77], v146 offset:18432
	ds_read_b128 v[78:81], v146 offset:19456
	ds_read_b128 v[82:85], v146 offset:20480
	ds_read_b128 v[86:89], v146 offset:21504
	ds_read_b128 v[90:93], v146 offset:22528
	ds_read_b128 v[94:97], v146 offset:23552
	buffer_load_dwordx4 v143, s[12:15], s78 offen lds
	s_add_i32 s79, s78, 0x20000
	s_mov_b32 m0, s36
	s_nop 0
	buffer_load_dwordx4 v143, s[12:15], s79 offen lds
	s_add_i32 s79, s78, 0x40000
	s_mov_b32 m0, s37
	s_nop 0
	buffer_load_dwordx4 v143, s[12:15], s79 offen lds
	s_add_i32 s79, s78, 0x60000
	s_mov_b32 m0, s38
	s_nop 0
	buffer_load_dwordx4 v143, s[12:15], s79 offen lds
	s_mov_b32 m0, s3
	s_add_i32 s79, s76, 0x20000
	buffer_load_dwordx4 v142, s[12:15], s76 offen lds
	s_mov_b32 m0, s39
	s_nop 0
	buffer_load_dwordx4 v142, s[12:15], s79 offen lds
	s_waitcnt vmcnt(8)
	s_waitcnt lgkmcnt(0)
	s_barrier
	s_setprio 1
	s_waitcnt lgkmcnt(6)
	v_mfma_scale_f32_16x16x128_f8f6f4 v[62:65], v[132:139], v[66:73], v[62:65], v148, v147 op_sel_hi:[0,0,0]
	v_mfma_scale_f32_16x16x128_f8f6f4 v[58:61], v[152:159], v[66:73], v[58:61], v148, v147 op_sel_hi:[0,0,0]
	s_waitcnt lgkmcnt(4)
	v_mfma_scale_f32_16x16x128_f8f6f4 v[54:57], v[132:139], v[74:81], v[54:57], v148, v147 op_sel_hi:[0,0,0]
	v_mfma_scale_f32_16x16x128_f8f6f4 v[50:53], v[152:159], v[74:81], v[50:53], v148, v147 op_sel_hi:[0,0,0]
	s_waitcnt lgkmcnt(2)
	v_mfma_scale_f32_16x16x128_f8f6f4 v[200:203], v[132:139], v[82:89], v[38:41], v148, v147 op_sel_hi:[0,0,0]
	v_mfma_scale_f32_16x16x128_f8f6f4 v[204:207], v[152:159], v[82:89], v[34:37], v148, v147 op_sel_hi:[0,0,0]
	s_waitcnt lgkmcnt(0)
	v_mfma_scale_f32_16x16x128_f8f6f4 v[216:219], v[132:139], v[90:97], v[22:25], v148, v147 op_sel_hi:[0,0,0]
	v_mfma_scale_f32_16x16x128_f8f6f4 v[220:223], v[152:159], v[90:97], v[18:21], v148, v147 op_sel_hi:[0,0,0]
	s_setprio 0
	s_setprio 1
	v_mfma_scale_f32_16x16x128_f8f6f4 v[224:227], v[160:167], v[66:73], v[46:49], v148, v147 op_sel_hi:[0,0,0]
	v_mfma_scale_f32_16x16x128_f8f6f4 v[228:231], v[168:175], v[66:73], v[42:45], v148, v147 op_sel_hi:[0,0,0]
	v_mfma_scale_f32_16x16x128_f8f6f4 v[232:235], v[160:167], v[74:81], v[30:33], v148, v147 op_sel_hi:[0,0,0]
	v_mfma_scale_f32_16x16x128_f8f6f4 v[236:239], v[168:175], v[74:81], v[26:29], v148, v147 op_sel_hi:[0,0,0]
	v_mfma_scale_f32_16x16x128_f8f6f4 v[240:243], v[160:167], v[82:89], v[14:17], v148, v147 op_sel_hi:[0,0,0]
	v_mfma_scale_f32_16x16x128_f8f6f4 v[244:247], v[168:175], v[82:89], v[10:13], v148, v147 op_sel_hi:[0,0,0]
	v_mfma_scale_f32_16x16x128_f8f6f4 v[248:251], v[160:167], v[90:97], v[6:9], v148, v147 op_sel_hi:[0,0,0]
	v_mfma_scale_f32_16x16x128_f8f6f4 v[252:255], v[168:175], v[90:97], v[2:5], v148, v147 op_sel_hi:[0,0,0]
	s_setprio 0
	s_barrier
	s_nop 4
	ds_read_b128 v[2:5], v149
	ds_read_b128 v[6:9], v149 offset:1024
	ds_read_b128 v[10:13], v149 offset:2048
	ds_read_b128 v[14:17], v149 offset:3072
	ds_read_b128 v[132:135], v150
	ds_read_b128 v[136:139], v150 offset:1024
	ds_read_b128 v[152:155], v150 offset:2048
	ds_read_b128 v[156:159], v150 offset:3072
	s_mov_b32 m0, s40
	s_add_i32 s79, s76, 0x40000
	ds_read_b128 v[18:21], v146 offset:32768
	ds_read_b128 v[22:25], v146 offset:33792
	ds_read_b128 v[26:29], v146 offset:34816
	ds_read_b128 v[30:33], v146 offset:35840
	ds_read_b128 v[34:37], v146 offset:36864
	ds_read_b128 v[38:41], v146 offset:37888
	ds_read_b128 v[42:45], v146 offset:38912
	ds_read_b128 v[46:49], v146 offset:39936
	buffer_load_dwordx4 v142, s[12:15], s79 offen lds
	s_add_i32 s79, s76, 0x60000
	s_mov_b32 m0, s41
	s_nop 0
	buffer_load_dwordx4 v142, s[12:15], s79 offen lds
	s_waitcnt vmcnt(8)
	s_waitcnt lgkmcnt(0)
	s_barrier
	s_setprio 1
	s_waitcnt lgkmcnt(6)
	v_mfma_scale_f32_16x16x128_f8f6f4 v[126:129], v[2:9], v[18:25], v[126:129], v148, v147 op_sel_hi:[0,0,0]
	v_mfma_scale_f32_16x16x128_f8f6f4 v[122:125], v[10:17], v[18:25], v[122:125], v148, v147 op_sel_hi:[0,0,0]
	s_waitcnt lgkmcnt(4)
	v_mfma_scale_f32_16x16x128_f8f6f4 v[118:121], v[2:9], v[26:33], v[118:121], v148, v147 op_sel_hi:[0,0,0]
	v_mfma_scale_f32_16x16x128_f8f6f4 v[114:117], v[10:17], v[26:33], v[114:117], v148, v147 op_sel_hi:[0,0,0]
	s_waitcnt lgkmcnt(2)
	v_mfma_scale_f32_16x16x128_f8f6f4 v[102:105], v[2:9], v[34:41], v[102:105], v148, v147 op_sel_hi:[0,0,0]
	v_mfma_scale_f32_16x16x128_f8f6f4 v[98:101], v[10:17], v[34:41], v[98:101], v148, v147 op_sel_hi:[0,0,0]
	s_waitcnt lgkmcnt(0)
	v_mfma_scale_f32_16x16x128_f8f6f4 v[86:89], v[2:9], v[42:49], v[208:211], v148, v147 op_sel_hi:[0,0,0]
	v_mfma_scale_f32_16x16x128_f8f6f4 v[82:85], v[10:17], v[42:49], v[212:215], v148, v147 op_sel_hi:[0,0,0]
	s_setprio 0
	s_setprio 1
	v_mfma_scale_f32_16x16x128_f8f6f4 v[110:113], v[132:139], v[18:25], v[110:113], v148, v147 op_sel_hi:[0,0,0]
	v_mfma_scale_f32_16x16x128_f8f6f4 v[106:109], v[152:159], v[18:25], v[106:109], v148, v147 op_sel_hi:[0,0,0]
	v_mfma_scale_f32_16x16x128_f8f6f4 v[94:97], v[132:139], v[26:33], v[176:179], v148, v147 op_sel_hi:[0,0,0]
	v_mfma_scale_f32_16x16x128_f8f6f4 v[90:93], v[152:159], v[26:33], v[180:183], v148, v147 op_sel_hi:[0,0,0]
	v_mfma_scale_f32_16x16x128_f8f6f4 v[78:81], v[132:139], v[34:41], v[184:187], v148, v147 op_sel_hi:[0,0,0]
	v_mfma_scale_f32_16x16x128_f8f6f4 v[74:77], v[152:159], v[34:41], v[188:191], v148, v147 op_sel_hi:[0,0,0]
	v_mfma_scale_f32_16x16x128_f8f6f4 v[70:73], v[132:139], v[42:49], v[192:195], v148, v147 op_sel_hi:[0,0,0]
	v_mfma_scale_f32_16x16x128_f8f6f4 v[66:69], v[152:159], v[42:49], v[196:199], v148, v147 op_sel_hi:[0,0,0]
	s_setprio 0
	s_barrier
	s_mov_b32 m0, s49
	s_add_i32 s79, s78, 0x80
	ds_read_b128 v[26:29], v146 offset:49152
	ds_read_b128 v[30:33], v146 offset:50176
	ds_read_b128 v[160:163], v146 offset:51200
	ds_read_b128 v[164:167], v146 offset:52224
	ds_read_b128 v[168:171], v146 offset:53248
	ds_read_b128 v[172:175], v146 offset:54272
	ds_read_b128 v[176:179], v146 offset:55296
	ds_read_b128 v[180:183], v146 offset:56320
	buffer_load_dwordx4 v143, s[12:15], s79 offen lds
	s_add_i32 s79, s78, 0x20080
	s_mov_b32 m0, s53
	s_add_i32 s76, s76, 0x20080
	buffer_load_dwordx4 v143, s[12:15], s79 offen lds
	s_add_i32 s79, s78, 0x40080
	s_mov_b32 m0, s56
	s_add_i32 s78, s78, 0x60080
	buffer_load_dwordx4 v143, s[12:15], s79 offen lds
	s_mov_b32 m0, s57
	s_nop 0
	buffer_load_dwordx4 v143, s[12:15], s78 offen lds
	s_mov_b32 m0, s54
	s_nop 0
	buffer_load_dwordx4 v142, s[12:15], s77 offen lds
	s_mov_b32 m0, s55
	s_nop 0
	buffer_load_dwordx4 v142, s[12:15], s76 offen lds
	s_waitcnt vmcnt(8)
	s_waitcnt lgkmcnt(0)
	s_barrier
	s_setprio 1
	s_waitcnt lgkmcnt(6)
	v_mfma_scale_f32_16x16x128_f8f6f4 v[62:65], v[2:9], v[26:33], v[62:65], v148, v147 op_sel_hi:[0,0,0]
	v_mfma_scale_f32_16x16x128_f8f6f4 v[58:61], v[10:17], v[26:33], v[58:61], v148, v147 op_sel_hi:[0,0,0]
	s_waitcnt lgkmcnt(4)
	v_mfma_scale_f32_16x16x128_f8f6f4 v[54:57], v[2:9], v[160:167], v[54:57], v148, v147 op_sel_hi:[0,0,0]
	v_mfma_scale_f32_16x16x128_f8f6f4 v[50:53], v[10:17], v[160:167], v[50:53], v148, v147 op_sel_hi:[0,0,0]
	s_waitcnt lgkmcnt(2)
	v_mfma_scale_f32_16x16x128_f8f6f4 v[38:41], v[2:9], v[168:175], v[200:203], v148, v147 op_sel_hi:[0,0,0]
	v_mfma_scale_f32_16x16x128_f8f6f4 v[34:37], v[10:17], v[168:175], v[204:207], v148, v147 op_sel_hi:[0,0,0]
	s_waitcnt lgkmcnt(0)
	v_mfma_scale_f32_16x16x128_f8f6f4 v[22:25], v[2:9], v[176:183], v[216:219], v148, v147 op_sel_hi:[0,0,0]
	v_mfma_scale_f32_16x16x128_f8f6f4 v[18:21], v[10:17], v[176:183], v[220:223], v148, v147 op_sel_hi:[0,0,0]
	s_setprio 0
	s_setprio 1
	v_mfma_scale_f32_16x16x128_f8f6f4 v[46:49], v[132:139], v[26:33], v[224:227], v148, v147 op_sel_hi:[0,0,0]
	v_mfma_scale_f32_16x16x128_f8f6f4 v[42:45], v[152:159], v[26:33], v[228:231], v148, v147 op_sel_hi:[0,0,0]
	v_mfma_scale_f32_16x16x128_f8f6f4 v[30:33], v[132:139], v[160:167], v[232:235], v148, v147 op_sel_hi:[0,0,0]
	v_mfma_scale_f32_16x16x128_f8f6f4 v[26:29], v[152:159], v[160:167], v[236:239], v148, v147 op_sel_hi:[0,0,0]
	v_mfma_scale_f32_16x16x128_f8f6f4 v[14:17], v[132:139], v[168:175], v[240:243], v148, v147 op_sel_hi:[0,0,0]
	v_mfma_scale_f32_16x16x128_f8f6f4 v[10:13], v[152:159], v[168:175], v[244:247], v148, v147 op_sel_hi:[0,0,0]
	v_mfma_scale_f32_16x16x128_f8f6f4 v[6:9], v[132:139], v[176:183], v[248:251], v148, v147 op_sel_hi:[0,0,0]
	v_mfma_scale_f32_16x16x128_f8f6f4 v[2:5], v[152:159], v[176:183], v[252:255], v148, v147 op_sel_hi:[0,0,0]
	s_setprio 0
	s_add_i32 s75, s75, 2
	s_addk_i32 s34, 0x100
	s_addk_i32 s35, 0x100
	s_cmp_gt_u32 s75, 13
	s_cbranch_scc0 .Lkbar4
	s_barrier
	s_and_b64 vcc, exec, s[20:21]
	s_cbranch_vccz .LBB0_264
	s_barrier

.LBB0_1819:
	s_add_i32 s6, s24, 0x30080
	s_add_i32 s7, s25, 0x100
	s_mov_b32 s24, -2
	s_branch .LBB0_1820

.LBB0_1820:
	v_add_u32_e32 v11, 0x10000, v231
	ds_read_b128 v[2:5], v11
	ds_read_b128 v[6:9], v11 offset:1024
	ds_read_b128 v[150:153], v11 offset:2048
	ds_read_b128 v[154:157], v11 offset:3072
	v_add_u32_e32 v11, 0x14000, v231
	ds_read_b128 v[158:161], v11
	ds_read_b128 v[162:165], v11 offset:1024
	ds_read_b128 v[166:169], v11 offset:2048
	ds_read_b128 v[170:173], v11 offset:3072
	s_add_i32 s8, s6, 0xfffd0080
	s_cmp_eq_u32 s24, 4
	s_cselect_b32 s25, s63, s8
	s_cselect_b32 s68, s64, s7
	s_add_i32 s67, s25, 0x80
	s_add_i32 s69, s6, 0xffff0000
	s_mov_b32 s8, s44
	s_mov_b32 m0, s43
	ds_read_b128 v[174:177], v232
	ds_read_b128 v[178:181], v232 offset:1024
	ds_read_b128 v[182:185], v232 offset:2048
	ds_read_b128 v[186:189], v232 offset:3072
	ds_read_b128 v[190:193], v232 offset:4096
	ds_read_b128 v[194:197], v232 offset:5120
	ds_read_b128 v[198:201], v232 offset:6144
	ds_read_b128 v[202:205], v232 offset:7168
	buffer_load_dwordx4 v1, s[8:11], s69 offen lds
	s_mov_b32 m0, s49
	s_nop 0
	buffer_load_dwordx4 v1, s[8:11], s6 offen lds
	s_waitcnt vmcnt(8)
	s_waitcnt lgkmcnt(0)
	s_barrier
	s_setprio 1
	s_waitcnt lgkmcnt(6)
	v_mfma_scale_f32_16x16x128_f8f6f4 v[138:141], v[2:9], v[174:181], v[138:141], v233, v233 op_sel_hi:[0,0,0]
	v_mfma_scale_f32_16x16x128_f8f6f4 v[134:137], v[150:157], v[174:181], v[134:137], v233, v233 op_sel_hi:[0,0,0]
	s_waitcnt lgkmcnt(4)
	v_mfma_scale_f32_16x16x128_f8f6f4 v[130:133], v[2:9], v[182:189], v[130:133], v233, v233 op_sel_hi:[0,0,0]
	v_mfma_scale_f32_16x16x128_f8f6f4 v[126:129], v[150:157], v[182:189], v[126:129], v233, v233 op_sel_hi:[0,0,0]
	s_waitcnt lgkmcnt(2)
	v_mfma_scale_f32_16x16x128_f8f6f4 v[122:125], v[2:9], v[190:197], v[122:125], v233, v233 op_sel_hi:[0,0,0]
	v_mfma_scale_f32_16x16x128_f8f6f4 v[118:121], v[150:157], v[190:197], v[118:121], v233, v233 op_sel_hi:[0,0,0]
	s_waitcnt lgkmcnt(0)
	v_mfma_scale_f32_16x16x128_f8f6f4 v[114:117], v[2:9], v[198:205], v[114:117], v233, v233 op_sel_hi:[0,0,0]
	v_mfma_scale_f32_16x16x128_f8f6f4 v[110:113], v[150:157], v[198:205], v[110:113], v233, v233 op_sel_hi:[0,0,0]
	s_setprio 0
	s_setprio 1
	v_mfma_scale_f32_16x16x128_f8f6f4 v[142:145], v[158:165], v[174:181], v[106:109], v233, v233 op_sel_hi:[0,0,0]
	v_mfma_scale_f32_16x16x128_f8f6f4 v[174:177], v[166:173], v[174:181], v[102:105], v233, v233 op_sel_hi:[0,0,0]
	v_mfma_scale_f32_16x16x128_f8f6f4 v[178:181], v[158:165], v[182:189], v[98:101], v233, v233 op_sel_hi:[0,0,0]
	v_mfma_scale_f32_16x16x128_f8f6f4 v[182:185], v[166:173], v[182:189], v[94:97], v233, v233 op_sel_hi:[0,0,0]
	v_mfma_scale_f32_16x16x128_f8f6f4 v[186:189], v[158:165], v[190:197], v[90:93], v233, v233 op_sel_hi:[0,0,0]
	v_mfma_scale_f32_16x16x128_f8f6f4 v[190:193], v[166:173], v[190:197], v[86:89], v233, v233 op_sel_hi:[0,0,0]
	v_mfma_scale_f32_16x16x128_f8f6f4 v[194:197], v[158:165], v[198:205], v[82:85], v233, v233 op_sel_hi:[0,0,0]
	v_mfma_scale_f32_16x16x128_f8f6f4 v[198:201], v[166:173], v[198:205], v[78:81], v233, v233 op_sel_hi:[0,0,0]
	s_setprio 0
	s_barrier
	s_mov_b32 m0, s26
	s_nop 3
	ds_read_b128 v[78:81], v232 offset:16384
	ds_read_b128 v[82:85], v232 offset:17408
	ds_read_b128 v[86:89], v232 offset:18432
	ds_read_b128 v[90:93], v232 offset:19456
	ds_read_b128 v[94:97], v232 offset:20480
	ds_read_b128 v[98:101], v232 offset:21504
	ds_read_b128 v[102:105], v232 offset:22528
	ds_read_b128 v[106:109], v232 offset:23552
	buffer_load_dwordx4 v230, s[8:11], s68 offen lds
	s_add_i32 s69, s68, 0x10000
	s_mov_b32 m0, s27
	s_nop 0
	buffer_load_dwordx4 v230, s[8:11], s69 offen lds
	s_add_i32 s69, s68, 0x20000
	s_mov_b32 m0, s28
	s_nop 0
	buffer_load_dwordx4 v230, s[8:11], s69 offen lds
	s_add_i32 s69, s68, 0x30000
	s_mov_b32 m0, s29
	s_nop 0
	buffer_load_dwordx4 v230, s[8:11], s69 offen lds
	s_mov_b32 m0, s3
	s_add_i32 s69, s25, 0x10000
	buffer_load_dwordx4 v1, s[8:11], s25 offen lds
	s_mov_b32 m0, s30
	s_nop 0
	buffer_load_dwordx4 v1, s[8:11], s69 offen lds
	s_waitcnt vmcnt(8)
	s_waitcnt lgkmcnt(0)
	s_barrier
	s_setprio 1
	s_waitcnt lgkmcnt(6)
	v_mfma_scale_f32_16x16x128_f8f6f4 v[74:77], v[2:9], v[78:85], v[74:77], v233, v233 op_sel_hi:[0,0,0]
	v_mfma_scale_f32_16x16x128_f8f6f4 v[70:73], v[150:157], v[78:85], v[70:73], v233, v233 op_sel_hi:[0,0,0]
	s_waitcnt lgkmcnt(4)
	v_mfma_scale_f32_16x16x128_f8f6f4 v[66:69], v[2:9], v[86:93], v[66:69], v233, v233 op_sel_hi:[0,0,0]
	v_mfma_scale_f32_16x16x128_f8f6f4 v[62:65], v[150:157], v[86:93], v[62:65], v233, v233 op_sel_hi:[0,0,0]
	s_waitcnt lgkmcnt(2)
	v_mfma_scale_f32_16x16x128_f8f6f4 v[58:61], v[2:9], v[94:101], v[58:61], v233, v233 op_sel_hi:[0,0,0]
	v_mfma_scale_f32_16x16x128_f8f6f4 v[54:57], v[150:157], v[94:101], v[54:57], v233, v233 op_sel_hi:[0,0,0]
	s_waitcnt lgkmcnt(0)
	v_mfma_scale_f32_16x16x128_f8f6f4 v[202:205], v[2:9], v[102:109], v[50:53], v233, v233 op_sel_hi:[0,0,0]
	v_mfma_scale_f32_16x16x128_f8f6f4 v[206:209], v[150:157], v[102:109], v[46:49], v233, v233 op_sel_hi:[0,0,0]
	s_setprio 0
	s_setprio 1
	v_mfma_scale_f32_16x16x128_f8f6f4 v[210:213], v[158:165], v[78:85], v[42:45], v233, v233 op_sel_hi:[0,0,0]
	v_mfma_scale_f32_16x16x128_f8f6f4 v[214:217], v[166:173], v[78:85], v[38:41], v233, v233 op_sel_hi:[0,0,0]
	v_mfma_scale_f32_16x16x128_f8f6f4 v[218:221], v[158:165], v[86:93], v[34:37], v233, v233 op_sel_hi:[0,0,0]
	v_mfma_scale_f32_16x16x128_f8f6f4 v[222:225], v[166:173], v[86:93], v[30:33], v233, v233 op_sel_hi:[0,0,0]
	v_mfma_scale_f32_16x16x128_f8f6f4 v[226:229], v[158:165], v[94:101], v[26:29], v233, v233 op_sel_hi:[0,0,0]
	v_mfma_scale_f32_16x16x128_f8f6f4 v[236:239], v[166:173], v[94:101], v[22:25], v233, v233 op_sel_hi:[0,0,0]
	v_mfma_scale_f32_16x16x128_f8f6f4 v[240:243], v[158:165], v[102:109], v[18:21], v233, v233 op_sel_hi:[0,0,0]
	v_mfma_scale_f32_16x16x128_f8f6f4 v[244:247], v[166:173], v[102:109], v[14:17], v233, v233 op_sel_hi:[0,0,0]
	s_setprio 0
	s_barrier
	v_add_u32_e32 v11, 0x18000, v231
	ds_read_b128 v[2:5], v11
	ds_read_b128 v[6:9], v11 offset:1024
	s_nop 1
	ds_read_b128 v[12:15], v11 offset:2048
	ds_read_b128 v[16:19], v11 offset:3072
	v_add_u32_e32 v11, 0x1c000, v231
	ds_read_b128 v[150:153], v11
	ds_read_b128 v[154:157], v11 offset:1024
	ds_read_b128 v[158:161], v11 offset:2048
	ds_read_b128 v[162:165], v11 offset:3072
	s_mov_b32 m0, s31
	s_add_i32 s69, s25, 0x20000
	ds_read_b128 v[20:23], v232 offset:32768
	ds_read_b128 v[24:27], v232 offset:33792
	ds_read_b128 v[28:31], v232 offset:34816
	ds_read_b128 v[32:35], v232 offset:35840
	ds_read_b128 v[36:39], v232 offset:36864
	ds_read_b128 v[40:43], v232 offset:37888
	ds_read_b128 v[44:47], v232 offset:38912
	ds_read_b128 v[48:51], v232 offset:39936
	buffer_load_dwordx4 v1, s[8:11], s69 offen lds
	s_add_i32 s69, s25, 0x30000
	s_mov_b32 m0, s34
	s_nop 0
	buffer_load_dwordx4 v1, s[8:11], s69 offen lds
	s_waitcnt vmcnt(8)
	s_waitcnt lgkmcnt(0)
	s_barrier
	s_setprio 1
	s_waitcnt lgkmcnt(6)
	v_mfma_scale_f32_16x16x128_f8f6f4 v[138:141], v[2:9], v[20:27], v[138:141], v233, v233 op_sel_hi:[0,0,0]
	v_mfma_scale_f32_16x16x128_f8f6f4 v[134:137], v[12:19], v[20:27], v[134:137], v233, v233 op_sel_hi:[0,0,0]
	s_waitcnt lgkmcnt(4)
	v_mfma_scale_f32_16x16x128_f8f6f4 v[130:133], v[2:9], v[28:35], v[130:133], v233, v233 op_sel_hi:[0,0,0]
	v_mfma_scale_f32_16x16x128_f8f6f4 v[126:129], v[12:19], v[28:35], v[126:129], v233, v233 op_sel_hi:[0,0,0]
	s_waitcnt lgkmcnt(2)
	v_mfma_scale_f32_16x16x128_f8f6f4 v[122:125], v[2:9], v[36:43], v[122:125], v233, v233 op_sel_hi:[0,0,0]
	v_mfma_scale_f32_16x16x128_f8f6f4 v[118:121], v[12:19], v[36:43], v[118:121], v233, v233 op_sel_hi:[0,0,0]
	s_waitcnt lgkmcnt(0)
	v_mfma_scale_f32_16x16x128_f8f6f4 v[114:117], v[2:9], v[44:51], v[114:117], v233, v233 op_sel_hi:[0,0,0]
	v_mfma_scale_f32_16x16x128_f8f6f4 v[110:113], v[12:19], v[44:51], v[110:113], v233, v233 op_sel_hi:[0,0,0]
	s_setprio 0
	s_setprio 1
	v_mfma_scale_f32_16x16x128_f8f6f4 v[106:109], v[150:157], v[20:27], v[142:145], v233, v233 op_sel_hi:[0,0,0]
	v_mfma_scale_f32_16x16x128_f8f6f4 v[102:105], v[158:165], v[20:27], v[174:177], v233, v233 op_sel_hi:[0,0,0]
	v_mfma_scale_f32_16x16x128_f8f6f4 v[98:101], v[150:157], v[28:35], v[178:181], v233, v233 op_sel_hi:[0,0,0]
	v_mfma_scale_f32_16x16x128_f8f6f4 v[94:97], v[158:165], v[28:35], v[182:185], v233, v233 op_sel_hi:[0,0,0]
	v_mfma_scale_f32_16x16x128_f8f6f4 v[90:93], v[150:157], v[36:43], v[186:189], v233, v233 op_sel_hi:[0,0,0]
	v_mfma_scale_f32_16x16x128_f8f6f4 v[86:89], v[158:165], v[36:43], v[190:193], v233, v233 op_sel_hi:[0,0,0]
	v_mfma_scale_f32_16x16x128_f8f6f4 v[82:85], v[150:157], v[44:51], v[194:197], v233, v233 op_sel_hi:[0,0,0]
	v_mfma_scale_f32_16x16x128_f8f6f4 v[78:81], v[158:165], v[44:51], v[198:201], v233, v233 op_sel_hi:[0,0,0]
	s_setprio 0
	s_barrier
	s_mov_b32 m0, s35
	s_add_i32 s69, s68, 0x80
	ds_read_b128 v[20:23], v232 offset:49152
	ds_read_b128 v[24:27], v232 offset:50176
	ds_read_b128 v[166:169], v232 offset:51200
	ds_read_b128 v[170:173], v232 offset:52224
	ds_read_b128 v[174:177], v232 offset:53248
	ds_read_b128 v[178:181], v232 offset:54272
	ds_read_b128 v[182:185], v232 offset:55296
	ds_read_b128 v[186:189], v232 offset:56320
	buffer_load_dwordx4 v230, s[8:11], s69 offen lds
	s_add_i32 s69, s68, 0x10080
	s_mov_b32 m0, s36
	s_add_i32 s25, s25, 0x10080
	buffer_load_dwordx4 v230, s[8:11], s69 offen lds
	s_add_i32 s69, s68, 0x20080
	s_mov_b32 m0, s39
	s_add_i32 s68, s68, 0x30080
	buffer_load_dwordx4 v230, s[8:11], s69 offen lds
	s_mov_b32 m0, s40
	s_nop 0
	buffer_load_dwordx4 v230, s[8:11], s68 offen lds
	s_mov_b32 m0, s37
	s_nop 0
	buffer_load_dwordx4 v1, s[8:11], s67 offen lds
	s_mov_b32 m0, s38
	s_nop 0
	buffer_load_dwordx4 v1, s[8:11], s25 offen lds
	s_waitcnt vmcnt(8)
	s_waitcnt lgkmcnt(0)
	s_barrier
	s_setprio 1
	s_waitcnt lgkmcnt(6)
	v_mfma_scale_f32_16x16x128_f8f6f4 v[74:77], v[2:9], v[20:27], v[74:77], v233, v233 op_sel_hi:[0,0,0]
	v_mfma_scale_f32_16x16x128_f8f6f4 v[70:73], v[12:19], v[20:27], v[70:73], v233, v233 op_sel_hi:[0,0,0]
	s_waitcnt lgkmcnt(4)
	v_mfma_scale_f32_16x16x128_f8f6f4 v[66:69], v[2:9], v[166:173], v[66:69], v233, v233 op_sel_hi:[0,0,0]
	v_mfma_scale_f32_16x16x128_f8f6f4 v[62:65], v[12:19], v[166:173], v[62:65], v233, v233 op_sel_hi:[0,0,0]
	s_waitcnt lgkmcnt(2)
	v_mfma_scale_f32_16x16x128_f8f6f4 v[58:61], v[2:9], v[174:181], v[58:61], v233, v233 op_sel_hi:[0,0,0]
	v_mfma_scale_f32_16x16x128_f8f6f4 v[54:57], v[12:19], v[174:181], v[54:57], v233, v233 op_sel_hi:[0,0,0]
	s_waitcnt lgkmcnt(0)
	v_mfma_scale_f32_16x16x128_f8f6f4 v[50:53], v[2:9], v[182:189], v[202:205], v233, v233 op_sel_hi:[0,0,0]
	v_mfma_scale_f32_16x16x128_f8f6f4 v[46:49], v[12:19], v[182:189], v[206:209], v233, v233 op_sel_hi:[0,0,0]
	s_setprio 0
	s_setprio 1
	v_mfma_scale_f32_16x16x128_f8f6f4 v[42:45], v[150:157], v[20:27], v[210:213], v233, v233 op_sel_hi:[0,0,0]
	v_mfma_scale_f32_16x16x128_f8f6f4 v[38:41], v[158:165], v[20:27], v[214:217], v233, v233 op_sel_hi:[0,0,0]
	v_mfma_scale_f32_16x16x128_f8f6f4 v[34:37], v[150:157], v[166:173], v[218:221], v233, v233 op_sel_hi:[0,0,0]
	v_mfma_scale_f32_16x16x128_f8f6f4 v[30:33], v[158:165], v[166:173], v[222:225], v233, v233 op_sel_hi:[0,0,0]
	v_mfma_scale_f32_16x16x128_f8f6f4 v[26:29], v[150:157], v[174:181], v[226:229], v233, v233 op_sel_hi:[0,0,0]
	v_mfma_scale_f32_16x16x128_f8f6f4 v[22:25], v[158:165], v[174:181], v[236:239], v233, v233 op_sel_hi:[0,0,0]
	v_mfma_scale_f32_16x16x128_f8f6f4 v[18:21], v[150:157], v[182:189], v[240:243], v233, v233 op_sel_hi:[0,0,0]
	v_mfma_scale_f32_16x16x128_f8f6f4 v[14:17], v[158:165], v[182:189], v[244:247], v233, v233 op_sel_hi:[0,0,0]
	s_setprio 0
	s_add_i32 s24, s24, 2
	s_addk_i32 s6, 0x100
	s_addk_i32 s7, 0x100
	s_cmp_gt_u32 s24, 5
	s_cbranch_scc0 .Lkbar3
	s_barrier
	s_and_b64 vcc, exec, s[20:21]
	s_cbranch_vccz .LBB0_1823
	s_barrier

.LBB0_2057:
	v_mov_b32_e32 v2, 0
	s_add_i32 s6, s67, 0x60080
	s_add_i32 s7, s65, 0x100
	s_mov_b32 s65, -2
	v_mov_b32_e32 v3, v2
	v_mov_b32_e32 v4, v2
	v_mov_b32_e32 v5, v2
	v_mov_b32_e32 v6, v2
	v_mov_b32_e32 v7, v2
	v_mov_b32_e32 v8, v2
	v_mov_b32_e32 v9, v2
	v_mov_b32_e32 v10, v2
	v_mov_b32_e32 v11, v2
	v_mov_b32_e32 v12, v2
	v_mov_b32_e32 v13, v2
	v_mov_b32_e32 v18, v2
	v_mov_b32_e32 v19, v2
	v_mov_b32_e32 v20, v2
	v_mov_b32_e32 v21, v2
	v_mov_b32_e32 v26, v2
	v_mov_b32_e32 v27, v2
	v_mov_b32_e32 v28, v2
	v_mov_b32_e32 v29, v2
	v_mov_b32_e32 v34, v2
	v_mov_b32_e32 v35, v2
	v_mov_b32_e32 v36, v2
	v_mov_b32_e32 v37, v2
	v_mov_b32_e32 v42, v2
	v_mov_b32_e32 v43, v2
	v_mov_b32_e32 v44, v2
	v_mov_b32_e32 v45, v2
	v_mov_b32_e32 v50, v2
	v_mov_b32_e32 v51, v2
	v_mov_b32_e32 v52, v2
	v_mov_b32_e32 v53, v2
	v_mov_b32_e32 v14, v2
	v_mov_b32_e32 v15, v2
	v_mov_b32_e32 v16, v2
	v_mov_b32_e32 v17, v2
	v_mov_b32_e32 v22, v2
	v_mov_b32_e32 v23, v2
	v_mov_b32_e32 v24, v2
	v_mov_b32_e32 v25, v2
	v_mov_b32_e32 v30, v2
	v_mov_b32_e32 v31, v2
	v_mov_b32_e32 v32, v2
	v_mov_b32_e32 v33, v2
	v_mov_b32_e32 v38, v2
	v_mov_b32_e32 v39, v2
	v_mov_b32_e32 v40, v2
	v_mov_b32_e32 v41, v2
	v_mov_b32_e32 v46, v2
	v_mov_b32_e32 v47, v2
	v_mov_b32_e32 v48, v2
	v_mov_b32_e32 v49, v2
	v_mov_b32_e32 v54, v2
	v_mov_b32_e32 v55, v2
	v_mov_b32_e32 v56, v2
	v_mov_b32_e32 v57, v2
	v_mov_b32_e32 v58, v2
	v_mov_b32_e32 v59, v2
	v_mov_b32_e32 v60, v2
	v_mov_b32_e32 v61, v2
	v_mov_b32_e32 v62, v2
	v_mov_b32_e32 v63, v2
	v_mov_b32_e32 v64, v2
	v_mov_b32_e32 v65, v2
	v_mov_b32_e32 v66, v2
	v_mov_b32_e32 v67, v2
	v_mov_b32_e32 v68, v2
	v_mov_b32_e32 v69, v2
	v_mov_b32_e32 v70, v2
	v_mov_b32_e32 v71, v2
	v_mov_b32_e32 v72, v2
	v_mov_b32_e32 v73, v2
	v_mov_b32_e32 v74, v2
	v_mov_b32_e32 v75, v2
	v_mov_b32_e32 v76, v2
	v_mov_b32_e32 v77, v2
	v_mov_b32_e32 v82, v2
	v_mov_b32_e32 v83, v2
	v_mov_b32_e32 v84, v2
	v_mov_b32_e32 v85, v2
	v_mov_b32_e32 v90, v2
	v_mov_b32_e32 v91, v2
	v_mov_b32_e32 v92, v2
	v_mov_b32_e32 v93, v2
	v_mov_b32_e32 v98, v2
	v_mov_b32_e32 v99, v2
	v_mov_b32_e32 v100, v2
	v_mov_b32_e32 v101, v2
	v_mov_b32_e32 v106, v2
	v_mov_b32_e32 v107, v2
	v_mov_b32_e32 v108, v2
	v_mov_b32_e32 v109, v2
	v_mov_b32_e32 v114, v2
	v_mov_b32_e32 v115, v2
	v_mov_b32_e32 v116, v2
	v_mov_b32_e32 v117, v2
	v_mov_b32_e32 v78, v2
	v_mov_b32_e32 v79, v2
	v_mov_b32_e32 v80, v2
	v_mov_b32_e32 v81, v2
	v_mov_b32_e32 v86, v2
	v_mov_b32_e32 v87, v2
	v_mov_b32_e32 v88, v2
	v_mov_b32_e32 v89, v2
	v_mov_b32_e32 v94, v2
	v_mov_b32_e32 v95, v2
	v_mov_b32_e32 v96, v2
	v_mov_b32_e32 v97, v2
	v_mov_b32_e32 v102, v2
	v_mov_b32_e32 v103, v2
	v_mov_b32_e32 v104, v2
	v_mov_b32_e32 v105, v2
	v_mov_b32_e32 v110, v2
	v_mov_b32_e32 v111, v2
	v_mov_b32_e32 v112, v2
	v_mov_b32_e32 v113, v2
	v_mov_b32_e32 v118, v2
	v_mov_b32_e32 v119, v2
	v_mov_b32_e32 v120, v2
	v_mov_b32_e32 v121, v2
	v_mov_b32_e32 v122, v2
	v_mov_b32_e32 v123, v2
	v_mov_b32_e32 v124, v2
	v_mov_b32_e32 v125, v2
	v_mov_b32_e32 v126, v2
	v_mov_b32_e32 v127, v2
	v_mov_b32_e32 v128, v2
	v_mov_b32_e32 v129, v2
	s_branch .LBB0_2058

.LBB0_2058:
	ds_read_b128 v[146:149], v138
	ds_read_b128 v[150:153], v138 offset:1024
	ds_read_b128 v[154:157], v138 offset:2048
	ds_read_b128 v[158:161], v138 offset:3072
	ds_read_b128 v[162:165], v139
	ds_read_b128 v[166:169], v139 offset:1024
	ds_read_b128 v[170:173], v139 offset:2048
	ds_read_b128 v[174:177], v139 offset:3072
	s_add_i32 s67, s6, 0xfffa0080
	s_cmp_eq_u32 s65, 12
	s_cselect_b32 s67, s63, s67
	s_cselect_b32 s69, s64, s7
	s_add_i32 s68, s67, 0x80
	s_add_i32 s70, s6, 0xfffe0000
	s_mov_b32 m0, s56
	ds_read_b128 v[178:181], v140
	ds_read_b128 v[182:185], v140 offset:1024
	ds_read_b128 v[186:189], v140 offset:2048
	ds_read_b128 v[190:193], v140 offset:3072
	ds_read_b128 v[194:197], v140 offset:4096
	ds_read_b128 v[198:201], v140 offset:5120
	ds_read_b128 v[202:205], v140 offset:6144
	ds_read_b128 v[206:209], v140 offset:7168
	buffer_load_dwordx4 v1, s[8:11], s70 offen lds
	s_mov_b32 m0, s57
	s_nop 0
	buffer_load_dwordx4 v1, s[8:11], s6 offen lds
	s_waitcnt vmcnt(8)
	s_waitcnt lgkmcnt(0)
	s_barrier
	s_setprio 1
	s_waitcnt lgkmcnt(6)
	v_mfma_scale_f32_16x16x128_f8f6f4 v[126:129], v[146:153], v[178:185], v[126:129], v142, v141 op_sel_hi:[0,0,0]
	v_mfma_scale_f32_16x16x128_f8f6f4 v[122:125], v[154:161], v[178:185], v[122:125], v142, v141 op_sel_hi:[0,0,0]
	s_waitcnt lgkmcnt(4)
	v_mfma_scale_f32_16x16x128_f8f6f4 v[118:121], v[146:153], v[186:193], v[118:121], v142, v141 op_sel_hi:[0,0,0]
	v_mfma_scale_f32_16x16x128_f8f6f4 v[110:113], v[154:161], v[186:193], v[110:113], v142, v141 op_sel_hi:[0,0,0]
	s_waitcnt lgkmcnt(2)
	v_mfma_scale_f32_16x16x128_f8f6f4 v[102:105], v[146:153], v[194:201], v[102:105], v142, v141 op_sel_hi:[0,0,0]
	v_mfma_scale_f32_16x16x128_f8f6f4 v[130:133], v[154:161], v[194:201], v[94:97], v142, v141 op_sel_hi:[0,0,0]
	s_waitcnt lgkmcnt(0)
	v_mfma_scale_f32_16x16x128_f8f6f4 v[210:213], v[146:153], v[202:209], v[86:89], v142, v141 op_sel_hi:[0,0,0]
	v_mfma_scale_f32_16x16x128_f8f6f4 v[214:217], v[154:161], v[202:209], v[78:81], v142, v141 op_sel_hi:[0,0,0]
	s_setprio 0
	s_setprio 1
	v_mfma_scale_f32_16x16x128_f8f6f4 v[114:117], v[162:169], v[178:185], v[114:117], v142, v141 op_sel_hi:[0,0,0]
	v_mfma_scale_f32_16x16x128_f8f6f4 v[106:109], v[170:177], v[178:185], v[106:109], v142, v141 op_sel_hi:[0,0,0]
	v_mfma_scale_f32_16x16x128_f8f6f4 v[98:101], v[162:169], v[186:193], v[98:101], v142, v141 op_sel_hi:[0,0,0]
	v_mfma_scale_f32_16x16x128_f8f6f4 v[178:181], v[170:177], v[186:193], v[90:93], v142, v141 op_sel_hi:[0,0,0]
	v_mfma_scale_f32_16x16x128_f8f6f4 v[182:185], v[162:169], v[194:201], v[82:85], v142, v141 op_sel_hi:[0,0,0]
	v_mfma_scale_f32_16x16x128_f8f6f4 v[186:189], v[170:177], v[194:201], v[74:77], v142, v141 op_sel_hi:[0,0,0]
	v_mfma_scale_f32_16x16x128_f8f6f4 v[190:193], v[162:169], v[202:209], v[70:73], v142, v141 op_sel_hi:[0,0,0]
	v_mfma_scale_f32_16x16x128_f8f6f4 v[194:197], v[170:177], v[202:209], v[66:69], v142, v141 op_sel_hi:[0,0,0]
	s_setprio 0
	s_barrier
	s_mov_b32 m0, s30
	s_nop 3
	ds_read_b128 v[66:69], v140 offset:16384
	ds_read_b128 v[70:73], v140 offset:17408
	ds_read_b128 v[74:77], v140 offset:18432
	ds_read_b128 v[78:81], v140 offset:19456
	ds_read_b128 v[82:85], v140 offset:20480
	ds_read_b128 v[86:89], v140 offset:21504
	ds_read_b128 v[90:93], v140 offset:22528
	ds_read_b128 v[94:97], v140 offset:23552
	buffer_load_dwordx4 v136, s[8:11], s69 offen lds
	s_add_i32 s70, s69, 0x20000
	s_mov_b32 m0, s31
	s_nop 0
	buffer_load_dwordx4 v136, s[8:11], s70 offen lds
	s_add_i32 s70, s69, 0x40000
	s_mov_b32 m0, s34
	s_nop 0
	buffer_load_dwordx4 v136, s[8:11], s70 offen lds
	s_add_i32 s70, s69, 0x60000
	s_mov_b32 m0, s35
	s_nop 0
	buffer_load_dwordx4 v136, s[8:11], s70 offen lds
	s_mov_b32 m0, s3
	s_add_i32 s70, s67, 0x20000
	buffer_load_dwordx4 v1, s[8:11], s67 offen lds
	s_mov_b32 m0, s36
	s_nop 0
	buffer_load_dwordx4 v1, s[8:11], s70 offen lds
	s_waitcnt vmcnt(8)
	s_waitcnt lgkmcnt(0)
	s_barrier
	s_setprio 1
	s_waitcnt lgkmcnt(6)
	v_mfma_scale_f32_16x16x128_f8f6f4 v[62:65], v[146:153], v[66:73], v[62:65], v142, v141 op_sel_hi:[0,0,0]
	v_mfma_scale_f32_16x16x128_f8f6f4 v[58:61], v[154:161], v[66:73], v[58:61], v142, v141 op_sel_hi:[0,0,0]
	s_waitcnt lgkmcnt(4)
	v_mfma_scale_f32_16x16x128_f8f6f4 v[54:57], v[146:153], v[74:81], v[54:57], v142, v141 op_sel_hi:[0,0,0]
	v_mfma_scale_f32_16x16x128_f8f6f4 v[198:201], v[154:161], v[74:81], v[46:49], v142, v141 op_sel_hi:[0,0,0]
	s_waitcnt lgkmcnt(2)
	v_mfma_scale_f32_16x16x128_f8f6f4 v[202:205], v[146:153], v[82:89], v[38:41], v142, v141 op_sel_hi:[0,0,0]
	v_mfma_scale_f32_16x16x128_f8f6f4 v[206:209], v[154:161], v[82:89], v[30:33], v142, v141 op_sel_hi:[0,0,0]
	s_waitcnt lgkmcnt(0)
	v_mfma_scale_f32_16x16x128_f8f6f4 v[218:221], v[146:153], v[90:97], v[22:25], v142, v141 op_sel_hi:[0,0,0]
	v_mfma_scale_f32_16x16x128_f8f6f4 v[222:225], v[154:161], v[90:97], v[14:17], v142, v141 op_sel_hi:[0,0,0]
	s_setprio 0
	s_setprio 1
	v_mfma_scale_f32_16x16x128_f8f6f4 v[50:53], v[162:169], v[66:73], v[50:53], v142, v141 op_sel_hi:[0,0,0]
	v_mfma_scale_f32_16x16x128_f8f6f4 v[226:229], v[170:177], v[66:73], v[42:45], v142, v141 op_sel_hi:[0,0,0]
	v_mfma_scale_f32_16x16x128_f8f6f4 v[230:233], v[162:169], v[74:81], v[34:37], v142, v141 op_sel_hi:[0,0,0]
	v_mfma_scale_f32_16x16x128_f8f6f4 v[234:237], v[170:177], v[74:81], v[26:29], v142, v141 op_sel_hi:[0,0,0]
	v_mfma_scale_f32_16x16x128_f8f6f4 v[238:241], v[162:169], v[82:89], v[18:21], v142, v141 op_sel_hi:[0,0,0]
	v_mfma_scale_f32_16x16x128_f8f6f4 v[242:245], v[170:177], v[82:89], v[10:13], v142, v141 op_sel_hi:[0,0,0]
	v_mfma_scale_f32_16x16x128_f8f6f4 v[246:249], v[162:169], v[90:97], v[6:9], v142, v141 op_sel_hi:[0,0,0]
	v_mfma_scale_f32_16x16x128_f8f6f4 v[250:253], v[170:177], v[90:97], v[2:5], v142, v141 op_sel_hi:[0,0,0]
	s_setprio 0
	s_barrier
	s_nop 4
	ds_read_b128 v[2:5], v143
	ds_read_b128 v[6:9], v143 offset:1024
	ds_read_b128 v[10:13], v143 offset:2048
	ds_read_b128 v[14:17], v143 offset:3072
	ds_read_b128 v[146:149], v144
	ds_read_b128 v[150:153], v144 offset:1024
	ds_read_b128 v[154:157], v144 offset:2048
	ds_read_b128 v[158:161], v144 offset:3072
	s_mov_b32 m0, s37
	s_add_i32 s70, s67, 0x40000
	ds_read_b128 v[18:21], v140 offset:32768
	ds_read_b128 v[22:25], v140 offset:33792
	ds_read_b128 v[26:29], v140 offset:34816
	ds_read_b128 v[30:33], v140 offset:35840
	ds_read_b128 v[34:37], v140 offset:36864
	ds_read_b128 v[38:41], v140 offset:37888
	ds_read_b128 v[42:45], v140 offset:38912
	ds_read_b128 v[46:49], v140 offset:39936
	buffer_load_dwordx4 v1, s[8:11], s70 offen lds
	s_add_i32 s70, s67, 0x60000
	s_mov_b32 m0, s38
	s_nop 0
	buffer_load_dwordx4 v1, s[8:11], s70 offen lds
	s_waitcnt vmcnt(8)
	s_waitcnt lgkmcnt(0)
	s_barrier
	s_setprio 1
	s_waitcnt lgkmcnt(6)
	v_mfma_scale_f32_16x16x128_f8f6f4 v[126:129], v[2:9], v[18:25], v[126:129], v142, v141 op_sel_hi:[0,0,0]
	v_mfma_scale_f32_16x16x128_f8f6f4 v[122:125], v[10:17], v[18:25], v[122:125], v142, v141 op_sel_hi:[0,0,0]
	s_waitcnt lgkmcnt(4)
	v_mfma_scale_f32_16x16x128_f8f6f4 v[118:121], v[2:9], v[26:33], v[118:121], v142, v141 op_sel_hi:[0,0,0]
	v_mfma_scale_f32_16x16x128_f8f6f4 v[110:113], v[10:17], v[26:33], v[110:113], v142, v141 op_sel_hi:[0,0,0]
	s_waitcnt lgkmcnt(2)
	v_mfma_scale_f32_16x16x128_f8f6f4 v[102:105], v[2:9], v[34:41], v[102:105], v142, v141 op_sel_hi:[0,0,0]
	v_mfma_scale_f32_16x16x128_f8f6f4 v[94:97], v[10:17], v[34:41], v[130:133], v142, v141 op_sel_hi:[0,0,0]
	s_waitcnt lgkmcnt(0)
	v_mfma_scale_f32_16x16x128_f8f6f4 v[86:89], v[2:9], v[42:49], v[210:213], v142, v141 op_sel_hi:[0,0,0]
	v_mfma_scale_f32_16x16x128_f8f6f4 v[78:81], v[10:17], v[42:49], v[214:217], v142, v141 op_sel_hi:[0,0,0]
	s_setprio 0
	s_setprio 1
	v_mfma_scale_f32_16x16x128_f8f6f4 v[114:117], v[146:153], v[18:25], v[114:117], v142, v141 op_sel_hi:[0,0,0]
	v_mfma_scale_f32_16x16x128_f8f6f4 v[106:109], v[154:161], v[18:25], v[106:109], v142, v141 op_sel_hi:[0,0,0]
	v_mfma_scale_f32_16x16x128_f8f6f4 v[98:101], v[146:153], v[26:33], v[98:101], v142, v141 op_sel_hi:[0,0,0]
	v_mfma_scale_f32_16x16x128_f8f6f4 v[90:93], v[154:161], v[26:33], v[178:181], v142, v141 op_sel_hi:[0,0,0]
	v_mfma_scale_f32_16x16x128_f8f6f4 v[82:85], v[146:153], v[34:41], v[182:185], v142, v141 op_sel_hi:[0,0,0]
	v_mfma_scale_f32_16x16x128_f8f6f4 v[74:77], v[154:161], v[34:41], v[186:189], v142, v141 op_sel_hi:[0,0,0]
	v_mfma_scale_f32_16x16x128_f8f6f4 v[70:73], v[146:153], v[42:49], v[190:193], v142, v141 op_sel_hi:[0,0,0]
	v_mfma_scale_f32_16x16x128_f8f6f4 v[66:69], v[154:161], v[42:49], v[194:197], v142, v141 op_sel_hi:[0,0,0]
	s_setprio 0
	s_barrier
	s_mov_b32 m0, s40
	s_add_i32 s70, s69, 0x80
	ds_read_b128 v[162:165], v140 offset:49152
	ds_read_b128 v[166:169], v140 offset:50176
	ds_read_b128 v[170:173], v140 offset:51200
	ds_read_b128 v[174:177], v140 offset:52224
	ds_read_b128 v[178:181], v140 offset:53248
	ds_read_b128 v[182:185], v140 offset:54272
	ds_read_b128 v[186:189], v140 offset:55296
	ds_read_b128 v[190:193], v140 offset:56320
	buffer_load_dwordx4 v136, s[8:11], s70 offen lds
	s_add_i32 s70, s69, 0x20080
	s_mov_b32 m0, s41
	s_add_i32 s67, s67, 0x20080
	buffer_load_dwordx4 v136, s[8:11], s70 offen lds
	s_add_i32 s70, s69, 0x40080
	s_mov_b32 m0, s49
	s_add_i32 s69, s69, 0x60080
	buffer_load_dwordx4 v136, s[8:11], s70 offen lds
	s_mov_b32 m0, s53
	s_nop 0
	buffer_load_dwordx4 v136, s[8:11], s69 offen lds
	s_mov_b32 m0, s42
	s_nop 0
	buffer_load_dwordx4 v1, s[8:11], s68 offen lds
	s_mov_b32 m0, s43
	s_nop 0
	buffer_load_dwordx4 v1, s[8:11], s67 offen lds
	s_waitcnt vmcnt(8)
	s_waitcnt lgkmcnt(0)
	s_barrier
	s_setprio 1
	s_waitcnt lgkmcnt(6)
	v_mfma_scale_f32_16x16x128_f8f6f4 v[62:65], v[2:9], v[162:169], v[62:65], v142, v141 op_sel_hi:[0,0,0]
	v_mfma_scale_f32_16x16x128_f8f6f4 v[58:61], v[10:17], v[162:169], v[58:61], v142, v141 op_sel_hi:[0,0,0]
	s_waitcnt lgkmcnt(4)
	v_mfma_scale_f32_16x16x128_f8f6f4 v[54:57], v[2:9], v[170:177], v[54:57], v142, v141 op_sel_hi:[0,0,0]
	v_mfma_scale_f32_16x16x128_f8f6f4 v[46:49], v[10:17], v[170:177], v[198:201], v142, v141 op_sel_hi:[0,0,0]
	s_waitcnt lgkmcnt(2)
	v_mfma_scale_f32_16x16x128_f8f6f4 v[38:41], v[2:9], v[178:185], v[202:205], v142, v141 op_sel_hi:[0,0,0]
	v_mfma_scale_f32_16x16x128_f8f6f4 v[30:33], v[10:17], v[178:185], v[206:209], v142, v141 op_sel_hi:[0,0,0]
	s_waitcnt lgkmcnt(0)
	v_mfma_scale_f32_16x16x128_f8f6f4 v[22:25], v[2:9], v[186:193], v[218:221], v142, v141 op_sel_hi:[0,0,0]
	v_mfma_scale_f32_16x16x128_f8f6f4 v[14:17], v[10:17], v[186:193], v[222:225], v142, v141 op_sel_hi:[0,0,0]
	s_setprio 0
	s_setprio 1
	v_mfma_scale_f32_16x16x128_f8f6f4 v[50:53], v[146:153], v[162:169], v[50:53], v142, v141 op_sel_hi:[0,0,0]
	v_mfma_scale_f32_16x16x128_f8f6f4 v[42:45], v[154:161], v[162:169], v[226:229], v142, v141 op_sel_hi:[0,0,0]
	v_mfma_scale_f32_16x16x128_f8f6f4 v[34:37], v[146:153], v[170:177], v[230:233], v142, v141 op_sel_hi:[0,0,0]
	v_mfma_scale_f32_16x16x128_f8f6f4 v[26:29], v[154:161], v[170:177], v[234:237], v142, v141 op_sel_hi:[0,0,0]
	v_mfma_scale_f32_16x16x128_f8f6f4 v[18:21], v[146:153], v[178:185], v[238:241], v142, v141 op_sel_hi:[0,0,0]
	v_mfma_scale_f32_16x16x128_f8f6f4 v[10:13], v[154:161], v[178:185], v[242:245], v142, v141 op_sel_hi:[0,0,0]
	v_mfma_scale_f32_16x16x128_f8f6f4 v[6:9], v[146:153], v[186:193], v[246:249], v142, v141 op_sel_hi:[0,0,0]
	v_mfma_scale_f32_16x16x128_f8f6f4 v[2:5], v[154:161], v[186:193], v[250:253], v142, v141 op_sel_hi:[0,0,0]
	s_setprio 0
	s_add_i32 s65, s65, 2
	s_addk_i32 s6, 0x100
	s_addk_i32 s7, 0x100
	s_cmp_gt_u32 s65, 13
	s_cbranch_scc0 .Lkbar2
	s_barrier
	s_and_b64 vcc, exec, s[18:19]
	s_cbranch_vccz .LBB0_2061
	s_barrier

.LBB0_2335:
	v_mov_b32_e32 v2, 0
	s_add_i32 s62, s62, 0x60080
	s_addk_i32 s63, 0x100
	s_mov_b32 s64, -2
	v_mov_b32_e32 v3, v2
	v_mov_b32_e32 v4, v2
	v_mov_b32_e32 v5, v2
	v_mov_b32_e32 v6, v2
	v_mov_b32_e32 v7, v2
	v_mov_b32_e32 v8, v2
	v_mov_b32_e32 v9, v2
	v_mov_b32_e32 v10, v2
	v_mov_b32_e32 v11, v2
	v_mov_b32_e32 v12, v2
	v_mov_b32_e32 v13, v2
	v_mov_b32_e32 v14, v2
	v_mov_b32_e32 v15, v2
	v_mov_b32_e32 v16, v2
	v_mov_b32_e32 v17, v2
	v_mov_b32_e32 v18, v2
	v_mov_b32_e32 v19, v2
	v_mov_b32_e32 v20, v2
	v_mov_b32_e32 v21, v2
	v_mov_b32_e32 v22, v2
	v_mov_b32_e32 v23, v2
	v_mov_b32_e32 v24, v2
	v_mov_b32_e32 v25, v2
	v_mov_b32_e32 v26, v2
	v_mov_b32_e32 v27, v2
	v_mov_b32_e32 v28, v2
	v_mov_b32_e32 v29, v2
	v_mov_b32_e32 v30, v2
	v_mov_b32_e32 v31, v2
	v_mov_b32_e32 v32, v2
	v_mov_b32_e32 v33, v2
	v_mov_b32_e32 v66, v2
	v_mov_b32_e32 v67, v2
	v_mov_b32_e32 v68, v2
	v_mov_b32_e32 v69, v2
	v_mov_b32_e32 v70, v2
	v_mov_b32_e32 v71, v2
	v_mov_b32_e32 v72, v2
	v_mov_b32_e32 v73, v2
	v_mov_b32_e32 v74, v2
	v_mov_b32_e32 v75, v2
	v_mov_b32_e32 v76, v2
	v_mov_b32_e32 v77, v2
	v_mov_b32_e32 v78, v2
	v_mov_b32_e32 v79, v2
	v_mov_b32_e32 v80, v2
	v_mov_b32_e32 v81, v2
	v_mov_b32_e32 v82, v2
	v_mov_b32_e32 v83, v2
	v_mov_b32_e32 v84, v2
	v_mov_b32_e32 v85, v2
	v_mov_b32_e32 v86, v2
	v_mov_b32_e32 v87, v2
	v_mov_b32_e32 v88, v2
	v_mov_b32_e32 v89, v2
	v_mov_b32_e32 v90, v2
	v_mov_b32_e32 v91, v2
	v_mov_b32_e32 v92, v2
	v_mov_b32_e32 v93, v2
	v_mov_b32_e32 v94, v2
	v_mov_b32_e32 v95, v2
	v_mov_b32_e32 v96, v2
	v_mov_b32_e32 v97, v2
	v_mov_b32_e32 v34, v2
	v_mov_b32_e32 v35, v2
	v_mov_b32_e32 v36, v2
	v_mov_b32_e32 v37, v2
	v_mov_b32_e32 v38, v2
	v_mov_b32_e32 v39, v2
	v_mov_b32_e32 v40, v2
	v_mov_b32_e32 v41, v2
	v_mov_b32_e32 v42, v2
	v_mov_b32_e32 v43, v2
	v_mov_b32_e32 v44, v2
	v_mov_b32_e32 v45, v2
	v_mov_b32_e32 v46, v2
	v_mov_b32_e32 v47, v2
	v_mov_b32_e32 v48, v2
	v_mov_b32_e32 v49, v2
	v_mov_b32_e32 v50, v2
	v_mov_b32_e32 v51, v2
	v_mov_b32_e32 v52, v2
	v_mov_b32_e32 v53, v2
	v_mov_b32_e32 v54, v2
	v_mov_b32_e32 v55, v2
	v_mov_b32_e32 v56, v2
	v_mov_b32_e32 v57, v2
	v_mov_b32_e32 v58, v2
	v_mov_b32_e32 v59, v2
	v_mov_b32_e32 v60, v2
	v_mov_b32_e32 v61, v2
	v_mov_b32_e32 v62, v2
	v_mov_b32_e32 v63, v2
	v_mov_b32_e32 v64, v2
	v_mov_b32_e32 v65, v2
	v_mov_b32_e32 v98, v2
	v_mov_b32_e32 v99, v2
	v_mov_b32_e32 v100, v2
	v_mov_b32_e32 v101, v2
	v_mov_b32_e32 v102, v2
	v_mov_b32_e32 v103, v2
	v_mov_b32_e32 v104, v2
	v_mov_b32_e32 v105, v2
	v_mov_b32_e32 v114, v2
	v_mov_b32_e32 v115, v2
	v_mov_b32_e32 v116, v2
	v_mov_b32_e32 v117, v2
	v_mov_b32_e32 v118, v2
	v_mov_b32_e32 v119, v2
	v_mov_b32_e32 v120, v2
	v_mov_b32_e32 v121, v2
	v_mov_b32_e32 v122, v2
	v_mov_b32_e32 v123, v2
	v_mov_b32_e32 v124, v2
	v_mov_b32_e32 v125, v2
	v_mov_b32_e32 v126, v2
	v_mov_b32_e32 v127, v2
	v_mov_b32_e32 v128, v2
	v_mov_b32_e32 v129, v2
	v_mov_b32_e32 v130, v2
	v_mov_b32_e32 v131, v2
	v_mov_b32_e32 v132, v2
	v_mov_b32_e32 v133, v2
	v_mov_b32_e32 v134, v2
	v_mov_b32_e32 v135, v2
	v_mov_b32_e32 v136, v2
	v_mov_b32_e32 v137, v2
	s_branch .LBB0_2336

.LBB0_2336:
	ds_read_b128 v[106:109], v154
	ds_read_b128 v[110:113], v154 offset:1024
	ds_read_b128 v[138:141], v154 offset:2048
	ds_read_b128 v[142:145], v154 offset:3072
	ds_read_b128 v[162:165], v155
	ds_read_b128 v[166:169], v155 offset:1024
	ds_read_b128 v[170:173], v155 offset:2048
	ds_read_b128 v[174:177], v155 offset:3072
	s_add_i32 s65, s62, 0xfffa0080
	s_cmp_eq_u32 s64, 12
	s_cselect_b32 s65, s26, s65
	s_cselect_b32 s67, s27, s63
	s_add_i32 s66, s65, 0x80
	s_add_i32 s68, s62, 0xfffe0000
	s_mov_b32 m0, s53
	ds_read_b128 v[178:181], v156
	ds_read_b128 v[182:185], v156 offset:1024
	ds_read_b128 v[186:189], v156 offset:2048
	ds_read_b128 v[190:193], v156 offset:3072
	ds_read_b128 v[194:197], v156 offset:4096
	ds_read_b128 v[198:201], v156 offset:5120
	ds_read_b128 v[202:205], v156 offset:6144
	ds_read_b128 v[206:209], v156 offset:7168
	buffer_load_dwordx4 v1, s[8:11], s68 offen lds
	s_mov_b32 m0, s54
	s_nop 0
	buffer_load_dwordx4 v1, s[8:11], s62 offen lds
	s_waitcnt vmcnt(8)
	s_waitcnt lgkmcnt(0)
	s_barrier
	s_setprio 1
	s_waitcnt lgkmcnt(6)
	v_mfma_scale_f32_16x16x128_f8f6f4 v[134:137], v[106:113], v[178:185], v[134:137], v158, v157 op_sel_hi:[0,0,0]
	v_mfma_scale_f32_16x16x128_f8f6f4 v[130:133], v[138:145], v[178:185], v[130:133], v158, v157 op_sel_hi:[0,0,0]
	s_waitcnt lgkmcnt(4)
	v_mfma_scale_f32_16x16x128_f8f6f4 v[126:129], v[106:113], v[186:193], v[126:129], v158, v157 op_sel_hi:[0,0,0]
	v_mfma_scale_f32_16x16x128_f8f6f4 v[122:125], v[138:145], v[186:193], v[122:125], v158, v157 op_sel_hi:[0,0,0]
	s_waitcnt lgkmcnt(2)
	v_mfma_scale_f32_16x16x128_f8f6f4 v[118:121], v[106:113], v[194:201], v[118:121], v158, v157 op_sel_hi:[0,0,0]
	v_mfma_scale_f32_16x16x128_f8f6f4 v[114:117], v[138:145], v[194:201], v[114:117], v158, v157 op_sel_hi:[0,0,0]
	s_waitcnt lgkmcnt(0)
	v_mfma_scale_f32_16x16x128_f8f6f4 v[102:105], v[106:113], v[202:209], v[102:105], v158, v157 op_sel_hi:[0,0,0]
	v_mfma_scale_f32_16x16x128_f8f6f4 v[98:101], v[138:145], v[202:209], v[98:101], v158, v157 op_sel_hi:[0,0,0]
	s_setprio 0
	s_setprio 1
	v_mfma_scale_f32_16x16x128_f8f6f4 v[146:149], v[162:169], v[178:185], v[62:65], v158, v157 op_sel_hi:[0,0,0]
	v_mfma_scale_f32_16x16x128_f8f6f4 v[178:181], v[170:177], v[178:185], v[58:61], v158, v157 op_sel_hi:[0,0,0]
	v_mfma_scale_f32_16x16x128_f8f6f4 v[182:185], v[162:169], v[186:193], v[54:57], v158, v157 op_sel_hi:[0,0,0]
	v_mfma_scale_f32_16x16x128_f8f6f4 v[186:189], v[170:177], v[186:193], v[50:53], v158, v157 op_sel_hi:[0,0,0]
	v_mfma_scale_f32_16x16x128_f8f6f4 v[190:193], v[162:169], v[194:201], v[46:49], v158, v157 op_sel_hi:[0,0,0]
	v_mfma_scale_f32_16x16x128_f8f6f4 v[194:197], v[170:177], v[194:201], v[42:45], v158, v157 op_sel_hi:[0,0,0]
	v_mfma_scale_f32_16x16x128_f8f6f4 v[198:201], v[162:169], v[202:209], v[38:41], v158, v157 op_sel_hi:[0,0,0]
	v_mfma_scale_f32_16x16x128_f8f6f4 v[202:205], v[170:177], v[202:209], v[34:37], v158, v157 op_sel_hi:[0,0,0]
	s_setprio 0
	s_barrier
	s_mov_b32 m0, s23
	s_nop 3
	ds_read_b128 v[34:37], v156 offset:16384
	ds_read_b128 v[38:41], v156 offset:17408
	ds_read_b128 v[42:45], v156 offset:18432
	ds_read_b128 v[46:49], v156 offset:19456
	ds_read_b128 v[50:53], v156 offset:20480
	ds_read_b128 v[54:57], v156 offset:21504
	ds_read_b128 v[58:61], v156 offset:22528
	ds_read_b128 v[62:65], v156 offset:23552
	buffer_load_dwordx4 v152, s[8:11], s67 offen lds
	s_add_i32 s68, s67, 0x20000
	s_mov_b32 m0, s28
	s_nop 0
	buffer_load_dwordx4 v152, s[8:11], s68 offen lds
	s_add_i32 s68, s67, 0x40000
	s_mov_b32 m0, s29
	s_nop 0
	buffer_load_dwordx4 v152, s[8:11], s68 offen lds
	s_add_i32 s68, s67, 0x60000
	s_mov_b32 m0, s30
	s_nop 0
	buffer_load_dwordx4 v152, s[8:11], s68 offen lds
	s_mov_b32 m0, s3
	s_add_i32 s68, s65, 0x20000
	buffer_load_dwordx4 v1, s[8:11], s65 offen lds
	s_mov_b32 m0, s31
	s_nop 0
	buffer_load_dwordx4 v1, s[8:11], s68 offen lds
	s_waitcnt vmcnt(8)
	s_waitcnt lgkmcnt(0)
	s_barrier
	s_setprio 1
	s_waitcnt lgkmcnt(6)
	v_mfma_scale_f32_16x16x128_f8f6f4 v[94:97], v[106:113], v[34:41], v[94:97], v158, v157 op_sel_hi:[0,0,0]
	v_mfma_scale_f32_16x16x128_f8f6f4 v[90:93], v[138:145], v[34:41], v[90:93], v158, v157 op_sel_hi:[0,0,0]
	s_waitcnt lgkmcnt(4)
	v_mfma_scale_f32_16x16x128_f8f6f4 v[86:89], v[106:113], v[42:49], v[86:89], v158, v157 op_sel_hi:[0,0,0]
	v_mfma_scale_f32_16x16x128_f8f6f4 v[82:85], v[138:145], v[42:49], v[82:85], v158, v157 op_sel_hi:[0,0,0]
	s_waitcnt lgkmcnt(2)
	v_mfma_scale_f32_16x16x128_f8f6f4 v[78:81], v[106:113], v[50:57], v[78:81], v158, v157 op_sel_hi:[0,0,0]
	v_mfma_scale_f32_16x16x128_f8f6f4 v[74:77], v[138:145], v[50:57], v[74:77], v158, v157 op_sel_hi:[0,0,0]
	s_waitcnt lgkmcnt(0)
	v_mfma_scale_f32_16x16x128_f8f6f4 v[206:209], v[106:113], v[58:65], v[70:73], v158, v157 op_sel_hi:[0,0,0]
	v_mfma_scale_f32_16x16x128_f8f6f4 v[210:213], v[138:145], v[58:65], v[66:69], v158, v157 op_sel_hi:[0,0,0]
	s_setprio 0
	s_setprio 1
	v_mfma_scale_f32_16x16x128_f8f6f4 v[214:217], v[162:169], v[34:41], v[30:33], v158, v157 op_sel_hi:[0,0,0]
	v_mfma_scale_f32_16x16x128_f8f6f4 v[218:221], v[170:177], v[34:41], v[26:29], v158, v157 op_sel_hi:[0,0,0]
	v_mfma_scale_f32_16x16x128_f8f6f4 v[222:225], v[162:169], v[42:49], v[22:25], v158, v157 op_sel_hi:[0,0,0]
	v_mfma_scale_f32_16x16x128_f8f6f4 v[226:229], v[170:177], v[42:49], v[18:21], v158, v157 op_sel_hi:[0,0,0]
	v_mfma_scale_f32_16x16x128_f8f6f4 v[230:233], v[162:169], v[50:57], v[14:17], v158, v157 op_sel_hi:[0,0,0]
	v_mfma_scale_f32_16x16x128_f8f6f4 v[234:237], v[170:177], v[50:57], v[10:13], v158, v157 op_sel_hi:[0,0,0]
	v_mfma_scale_f32_16x16x128_f8f6f4 v[238:241], v[162:169], v[58:65], v[6:9], v158, v157 op_sel_hi:[0,0,0]
	v_mfma_scale_f32_16x16x128_f8f6f4 v[242:245], v[170:177], v[58:65], v[2:5], v158, v157 op_sel_hi:[0,0,0]
	s_setprio 0
	s_barrier
	s_nop 4
	ds_read_b128 v[2:5], v159
	ds_read_b128 v[6:9], v159 offset:1024
	ds_read_b128 v[10:13], v159 offset:2048
	ds_read_b128 v[14:17], v159 offset:3072
	ds_read_b128 v[106:109], v160
	ds_read_b128 v[110:113], v160 offset:1024
	ds_read_b128 v[138:141], v160 offset:2048
	ds_read_b128 v[142:145], v160 offset:3072
	s_mov_b32 m0, s34
	s_add_i32 s68, s65, 0x40000
	ds_read_b128 v[18:21], v156 offset:32768
	ds_read_b128 v[22:25], v156 offset:33792
	ds_read_b128 v[26:29], v156 offset:34816
	ds_read_b128 v[30:33], v156 offset:35840
	ds_read_b128 v[34:37], v156 offset:36864
	ds_read_b128 v[38:41], v156 offset:37888
	ds_read_b128 v[66:69], v156 offset:38912
	ds_read_b128 v[70:73], v156 offset:39936
	buffer_load_dwordx4 v1, s[8:11], s68 offen lds
	s_add_i32 s68, s65, 0x60000
	s_mov_b32 m0, s35
	s_nop 0
	buffer_load_dwordx4 v1, s[8:11], s68 offen lds
	s_waitcnt vmcnt(8)
	s_waitcnt lgkmcnt(0)
	s_barrier
	s_setprio 1
	s_waitcnt lgkmcnt(6)
	v_mfma_scale_f32_16x16x128_f8f6f4 v[134:137], v[2:9], v[18:25], v[134:137], v158, v157 op_sel_hi:[0,0,0]
	v_mfma_scale_f32_16x16x128_f8f6f4 v[130:133], v[10:17], v[18:25], v[130:133], v158, v157 op_sel_hi:[0,0,0]
	s_waitcnt lgkmcnt(4)
	v_mfma_scale_f32_16x16x128_f8f6f4 v[126:129], v[2:9], v[26:33], v[126:129], v158, v157 op_sel_hi:[0,0,0]
	v_mfma_scale_f32_16x16x128_f8f6f4 v[122:125], v[10:17], v[26:33], v[122:125], v158, v157 op_sel_hi:[0,0,0]
	s_waitcnt lgkmcnt(2)
	v_mfma_scale_f32_16x16x128_f8f6f4 v[118:121], v[2:9], v[34:41], v[118:121], v158, v157 op_sel_hi:[0,0,0]
	v_mfma_scale_f32_16x16x128_f8f6f4 v[114:117], v[10:17], v[34:41], v[114:117], v158, v157 op_sel_hi:[0,0,0]
	s_waitcnt lgkmcnt(0)
	v_mfma_scale_f32_16x16x128_f8f6f4 v[102:105], v[2:9], v[66:73], v[102:105], v158, v157 op_sel_hi:[0,0,0]
	v_mfma_scale_f32_16x16x128_f8f6f4 v[98:101], v[10:17], v[66:73], v[98:101], v158, v157 op_sel_hi:[0,0,0]
	s_setprio 0
	s_setprio 1
	v_mfma_scale_f32_16x16x128_f8f6f4 v[62:65], v[106:113], v[18:25], v[146:149], v158, v157 op_sel_hi:[0,0,0]
	v_mfma_scale_f32_16x16x128_f8f6f4 v[58:61], v[138:145], v[18:25], v[178:181], v158, v157 op_sel_hi:[0,0,0]
	v_mfma_scale_f32_16x16x128_f8f6f4 v[54:57], v[106:113], v[26:33], v[182:185], v158, v157 op_sel_hi:[0,0,0]
	v_mfma_scale_f32_16x16x128_f8f6f4 v[50:53], v[138:145], v[26:33], v[186:189], v158, v157 op_sel_hi:[0,0,0]
	v_mfma_scale_f32_16x16x128_f8f6f4 v[46:49], v[106:113], v[34:41], v[190:193], v158, v157 op_sel_hi:[0,0,0]
	v_mfma_scale_f32_16x16x128_f8f6f4 v[42:45], v[138:145], v[34:41], v[194:197], v158, v157 op_sel_hi:[0,0,0]
	v_mfma_scale_f32_16x16x128_f8f6f4 v[38:41], v[106:113], v[66:73], v[198:201], v158, v157 op_sel_hi:[0,0,0]
	v_mfma_scale_f32_16x16x128_f8f6f4 v[34:37], v[138:145], v[66:73], v[202:205], v158, v157 op_sel_hi:[0,0,0]
	s_setprio 0
	s_barrier
	s_mov_b32 m0, s36
	s_add_i32 s68, s67, 0x80
	ds_read_b128 v[18:21], v156 offset:49152
	ds_read_b128 v[22:25], v156 offset:50176
	ds_read_b128 v[162:165], v156 offset:51200
	ds_read_b128 v[166:169], v156 offset:52224
	ds_read_b128 v[170:173], v156 offset:53248
	ds_read_b128 v[174:177], v156 offset:54272
	ds_read_b128 v[178:181], v156 offset:55296
	ds_read_b128 v[182:185], v156 offset:56320
	buffer_load_dwordx4 v152, s[8:11], s68 offen lds
	s_add_i32 s68, s67, 0x20080
	s_mov_b32 m0, s37
	s_add_i32 s65, s65, 0x20080
	buffer_load_dwordx4 v152, s[8:11], s68 offen lds
	s_add_i32 s68, s67, 0x40080
	s_mov_b32 m0, s40
	s_add_i32 s67, s67, 0x60080
	buffer_load_dwordx4 v152, s[8:11], s68 offen lds
	s_mov_b32 m0, s41
	s_nop 0
	buffer_load_dwordx4 v152, s[8:11], s67 offen lds
	s_mov_b32 m0, s38
	s_nop 0
	buffer_load_dwordx4 v1, s[8:11], s66 offen lds
	s_mov_b32 m0, s39
	s_nop 0
	buffer_load_dwordx4 v1, s[8:11], s65 offen lds
	s_waitcnt vmcnt(8)
	s_waitcnt lgkmcnt(0)
	s_barrier
	s_setprio 1
	s_waitcnt lgkmcnt(6)
	v_mfma_scale_f32_16x16x128_f8f6f4 v[94:97], v[2:9], v[18:25], v[94:97], v158, v157 op_sel_hi:[0,0,0]
	v_mfma_scale_f32_16x16x128_f8f6f4 v[90:93], v[10:17], v[18:25], v[90:93], v158, v157 op_sel_hi:[0,0,0]
	s_waitcnt lgkmcnt(4)
	v_mfma_scale_f32_16x16x128_f8f6f4 v[86:89], v[2:9], v[162:169], v[86:89], v158, v157 op_sel_hi:[0,0,0]
	v_mfma_scale_f32_16x16x128_f8f6f4 v[82:85], v[10:17], v[162:169], v[82:85], v158, v157 op_sel_hi:[0,0,0]
	s_waitcnt lgkmcnt(2)
	v_mfma_scale_f32_16x16x128_f8f6f4 v[78:81], v[2:9], v[170:177], v[78:81], v158, v157 op_sel_hi:[0,0,0]
	v_mfma_scale_f32_16x16x128_f8f6f4 v[74:77], v[10:17], v[170:177], v[74:77], v158, v157 op_sel_hi:[0,0,0]
	s_waitcnt lgkmcnt(0)
	v_mfma_scale_f32_16x16x128_f8f6f4 v[70:73], v[2:9], v[178:185], v[206:209], v158, v157 op_sel_hi:[0,0,0]
	v_mfma_scale_f32_16x16x128_f8f6f4 v[66:69], v[10:17], v[178:185], v[210:213], v158, v157 op_sel_hi:[0,0,0]
	s_setprio 0
	s_setprio 1
	v_mfma_scale_f32_16x16x128_f8f6f4 v[30:33], v[106:113], v[18:25], v[214:217], v158, v157 op_sel_hi:[0,0,0]
	v_mfma_scale_f32_16x16x128_f8f6f4 v[26:29], v[138:145], v[18:25], v[218:221], v158, v157 op_sel_hi:[0,0,0]
	v_mfma_scale_f32_16x16x128_f8f6f4 v[22:25], v[106:113], v[162:169], v[222:225], v158, v157 op_sel_hi:[0,0,0]
	v_mfma_scale_f32_16x16x128_f8f6f4 v[18:21], v[138:145], v[162:169], v[226:229], v158, v157 op_sel_hi:[0,0,0]
	v_mfma_scale_f32_16x16x128_f8f6f4 v[14:17], v[106:113], v[170:177], v[230:233], v158, v157 op_sel_hi:[0,0,0]
	v_mfma_scale_f32_16x16x128_f8f6f4 v[10:13], v[138:145], v[170:177], v[234:237], v158, v157 op_sel_hi:[0,0,0]
	v_mfma_scale_f32_16x16x128_f8f6f4 v[6:9], v[106:113], v[178:185], v[238:241], v158, v157 op_sel_hi:[0,0,0]
	v_mfma_scale_f32_16x16x128_f8f6f4 v[2:5], v[138:145], v[178:185], v[242:245], v158, v157 op_sel_hi:[0,0,0]
	s_setprio 0
	s_add_i32 s64, s64, 2
	s_addk_i32 s62, 0x100
	s_addk_i32 s63, 0x100
	s_cmp_gt_u32 s64, 13
	s_cbranch_scc0 .Lkbar1
	s_barrier
	s_and_b64 vcc, exec, s[20:21]
	s_cbranch_vccz .LBB0_2339
	s_barrier

.LBB0_2425:
	v_mov_b32_e32 v2, 0
	s_add_i32 s8, s30, 0x60080
	s_add_i32 s9, s11, 0x100
	s_mov_b32 s11, -2
	v_mov_b32_e32 v3, v2
	v_mov_b32_e32 v4, v2
	v_mov_b32_e32 v5, v2
	v_mov_b32_e32 v6, v2
	v_mov_b32_e32 v7, v2
	v_mov_b32_e32 v8, v2
	v_mov_b32_e32 v9, v2
	v_mov_b32_e32 v10, v2
	v_mov_b32_e32 v11, v2
	v_mov_b32_e32 v12, v2
	v_mov_b32_e32 v13, v2
	v_mov_b32_e32 v14, v2
	v_mov_b32_e32 v15, v2
	v_mov_b32_e32 v16, v2
	v_mov_b32_e32 v17, v2
	v_mov_b32_e32 v18, v2
	v_mov_b32_e32 v19, v2
	v_mov_b32_e32 v20, v2
	v_mov_b32_e32 v21, v2
	v_mov_b32_e32 v22, v2
	v_mov_b32_e32 v23, v2
	v_mov_b32_e32 v24, v2
	v_mov_b32_e32 v25, v2
	v_mov_b32_e32 v26, v2
	v_mov_b32_e32 v27, v2
	v_mov_b32_e32 v28, v2
	v_mov_b32_e32 v29, v2
	v_mov_b32_e32 v30, v2
	v_mov_b32_e32 v31, v2
	v_mov_b32_e32 v32, v2
	v_mov_b32_e32 v33, v2
	v_mov_b32_e32 v34, v2
	v_mov_b32_e32 v35, v2
	v_mov_b32_e32 v36, v2
	v_mov_b32_e32 v37, v2
	v_mov_b32_e32 v38, v2
	v_mov_b32_e32 v39, v2
	v_mov_b32_e32 v40, v2
	v_mov_b32_e32 v41, v2
	v_mov_b32_e32 v42, v2
	v_mov_b32_e32 v43, v2
	v_mov_b32_e32 v44, v2
	v_mov_b32_e32 v45, v2
	v_mov_b32_e32 v46, v2
	v_mov_b32_e32 v47, v2
	v_mov_b32_e32 v48, v2
	v_mov_b32_e32 v49, v2
	v_mov_b32_e32 v50, v2
	v_mov_b32_e32 v51, v2
	v_mov_b32_e32 v52, v2
	v_mov_b32_e32 v53, v2
	v_mov_b32_e32 v54, v2
	v_mov_b32_e32 v55, v2
	v_mov_b32_e32 v56, v2
	v_mov_b32_e32 v57, v2
	v_mov_b32_e32 v58, v2
	v_mov_b32_e32 v59, v2
	v_mov_b32_e32 v60, v2
	v_mov_b32_e32 v61, v2
	v_mov_b32_e32 v62, v2
	v_mov_b32_e32 v63, v2
	v_mov_b32_e32 v64, v2
	v_mov_b32_e32 v65, v2
	v_mov_b32_e32 v66, v2
	v_mov_b32_e32 v67, v2
	v_mov_b32_e32 v68, v2
	v_mov_b32_e32 v69, v2
	v_mov_b32_e32 v70, v2
	v_mov_b32_e32 v71, v2
	v_mov_b32_e32 v72, v2
	v_mov_b32_e32 v73, v2
	v_mov_b32_e32 v74, v2
	v_mov_b32_e32 v75, v2
	v_mov_b32_e32 v76, v2
	v_mov_b32_e32 v77, v2
	v_mov_b32_e32 v78, v2
	v_mov_b32_e32 v79, v2
	v_mov_b32_e32 v80, v2
	v_mov_b32_e32 v81, v2
	v_mov_b32_e32 v82, v2
	v_mov_b32_e32 v83, v2
	v_mov_b32_e32 v84, v2
	v_mov_b32_e32 v85, v2
	v_mov_b32_e32 v86, v2
	v_mov_b32_e32 v87, v2
	v_mov_b32_e32 v88, v2
	v_mov_b32_e32 v89, v2
	v_mov_b32_e32 v90, v2
	v_mov_b32_e32 v91, v2
	v_mov_b32_e32 v92, v2
	v_mov_b32_e32 v93, v2
	v_mov_b32_e32 v94, v2
	v_mov_b32_e32 v95, v2
	v_mov_b32_e32 v96, v2
	v_mov_b32_e32 v97, v2
	v_mov_b32_e32 v98, v2
	v_mov_b32_e32 v99, v2
	v_mov_b32_e32 v100, v2
	v_mov_b32_e32 v101, v2
	v_mov_b32_e32 v102, v2
	v_mov_b32_e32 v103, v2
	v_mov_b32_e32 v104, v2
	v_mov_b32_e32 v105, v2
	v_mov_b32_e32 v106, v2
	v_mov_b32_e32 v107, v2
	v_mov_b32_e32 v108, v2
	v_mov_b32_e32 v109, v2
	v_mov_b32_e32 v110, v2
	v_mov_b32_e32 v111, v2
	v_mov_b32_e32 v112, v2
	v_mov_b32_e32 v113, v2
	v_mov_b32_e32 v114, v2
	v_mov_b32_e32 v115, v2
	v_mov_b32_e32 v116, v2
	v_mov_b32_e32 v117, v2
	v_mov_b32_e32 v118, v2
	v_mov_b32_e32 v119, v2
	v_mov_b32_e32 v120, v2
	v_mov_b32_e32 v121, v2
	v_mov_b32_e32 v122, v2
	v_mov_b32_e32 v123, v2
	v_mov_b32_e32 v124, v2
	v_mov_b32_e32 v125, v2
	v_mov_b32_e32 v126, v2
	v_mov_b32_e32 v127, v2
	v_mov_b32_e32 v128, v2
	v_mov_b32_e32 v129, v2
	s_branch .LBB0_2426

.LBB0_2426:
	ds_read_b128 v[130:133], v167
	ds_read_b128 v[134:137], v167 offset:1024
	ds_read_b128 v[138:141], v167 offset:2048
	ds_read_b128 v[142:145], v167 offset:3072
	ds_read_b128 v[148:151], v168
	ds_read_b128 v[152:155], v168 offset:1024
	ds_read_b128 v[156:159], v168 offset:2048
	ds_read_b128 v[160:163], v168 offset:3072
	s_add_i32 s30, s8, 0xfffa0080
	s_cmp_eq_u32 s11, 12
	s_cselect_b32 s30, s66, s30
	s_cselect_b32 s68, s67, s9
	s_add_i32 s31, s30, 0x80
	s_add_i32 s69, s8, 0xfffe0000
	s_mov_b32 m0, s58
	ds_read_b128 v[176:179], v169
	ds_read_b128 v[180:183], v169 offset:1024
	ds_read_b128 v[184:187], v169 offset:2048
	ds_read_b128 v[188:191], v169 offset:3072
	ds_read_b128 v[192:195], v169 offset:4096
	ds_read_b128 v[196:199], v169 offset:5120
	ds_read_b128 v[200:203], v169 offset:6144
	ds_read_b128 v[204:207], v169 offset:7168
	buffer_load_dwordx4 v1, s[12:15], s69 offen lds
	s_mov_b32 m0, s59
	s_nop 0
	buffer_load_dwordx4 v1, s[12:15], s8 offen lds
	s_waitcnt vmcnt(8)
	s_waitcnt lgkmcnt(0)
	s_barrier
	s_setprio 1
	s_waitcnt lgkmcnt(6)
	v_mfma_scale_f32_16x16x128_f8f6f4 v[126:129], v[130:137], v[176:183], v[126:129], v171, v170 op_sel_hi:[0,0,0]
	v_mfma_scale_f32_16x16x128_f8f6f4 v[122:125], v[138:145], v[176:183], v[122:125], v171, v170 op_sel_hi:[0,0,0]
	s_waitcnt lgkmcnt(4)
	v_mfma_scale_f32_16x16x128_f8f6f4 v[118:121], v[130:137], v[184:191], v[118:121], v171, v170 op_sel_hi:[0,0,0]
	v_mfma_scale_f32_16x16x128_f8f6f4 v[114:117], v[138:145], v[184:191], v[114:117], v171, v170 op_sel_hi:[0,0,0]
	s_waitcnt lgkmcnt(2)
	v_mfma_scale_f32_16x16x128_f8f6f4 v[110:113], v[130:137], v[192:199], v[110:113], v171, v170 op_sel_hi:[0,0,0]
	v_mfma_scale_f32_16x16x128_f8f6f4 v[106:109], v[138:145], v[192:199], v[106:109], v171, v170 op_sel_hi:[0,0,0]
	s_waitcnt lgkmcnt(0)
	v_mfma_scale_f32_16x16x128_f8f6f4 v[102:105], v[130:137], v[200:207], v[102:105], v171, v170 op_sel_hi:[0,0,0]
	v_mfma_scale_f32_16x16x128_f8f6f4 v[98:101], v[138:145], v[200:207], v[98:101], v171, v170 op_sel_hi:[0,0,0]
	s_setprio 0
	s_setprio 1
	v_mfma_scale_f32_16x16x128_f8f6f4 v[208:211], v[148:155], v[176:183], v[94:97], v171, v170 op_sel_hi:[0,0,0]
	v_mfma_scale_f32_16x16x128_f8f6f4 v[176:179], v[156:163], v[176:183], v[90:93], v171, v170 op_sel_hi:[0,0,0]
	v_mfma_scale_f32_16x16x128_f8f6f4 v[180:183], v[148:155], v[184:191], v[86:89], v171, v170 op_sel_hi:[0,0,0]
	v_mfma_scale_f32_16x16x128_f8f6f4 v[184:187], v[156:163], v[184:191], v[82:85], v171, v170 op_sel_hi:[0,0,0]
	v_mfma_scale_f32_16x16x128_f8f6f4 v[188:191], v[148:155], v[192:199], v[78:81], v171, v170 op_sel_hi:[0,0,0]
	v_mfma_scale_f32_16x16x128_f8f6f4 v[192:195], v[156:163], v[192:199], v[74:77], v171, v170 op_sel_hi:[0,0,0]
	v_mfma_scale_f32_16x16x128_f8f6f4 v[196:199], v[148:155], v[200:207], v[70:73], v171, v170 op_sel_hi:[0,0,0]
	v_mfma_scale_f32_16x16x128_f8f6f4 v[200:203], v[156:163], v[200:207], v[66:69], v171, v170 op_sel_hi:[0,0,0]
	s_setprio 0
	s_barrier
	s_mov_b32 m0, s34
	s_nop 3
	ds_read_b128 v[66:69], v169 offset:16384
	ds_read_b128 v[70:73], v169 offset:17408
	ds_read_b128 v[74:77], v169 offset:18432
	ds_read_b128 v[78:81], v169 offset:19456
	ds_read_b128 v[82:85], v169 offset:20480
	ds_read_b128 v[86:89], v169 offset:21504
	ds_read_b128 v[90:93], v169 offset:22528
	ds_read_b128 v[94:97], v169 offset:23552
	buffer_load_dwordx4 v165, s[12:15], s68 offen lds
	s_add_i32 s69, s68, 0x20000
	s_mov_b32 m0, s35
	s_nop 0
	buffer_load_dwordx4 v165, s[12:15], s69 offen lds
	s_add_i32 s69, s68, 0x40000
	s_mov_b32 m0, s36
	s_nop 0
	buffer_load_dwordx4 v165, s[12:15], s69 offen lds
	s_add_i32 s69, s68, 0x60000
	s_mov_b32 m0, s37
	s_nop 0
	buffer_load_dwordx4 v165, s[12:15], s69 offen lds
	s_mov_b32 m0, s3
	s_add_i32 s69, s30, 0x20000
	buffer_load_dwordx4 v1, s[12:15], s30 offen lds
	s_mov_b32 m0, s38
	s_nop 0
	buffer_load_dwordx4 v1, s[12:15], s69 offen lds
	s_waitcnt vmcnt(8)
	s_waitcnt lgkmcnt(0)
	s_barrier
	s_setprio 1
	s_waitcnt lgkmcnt(6)
	v_mfma_scale_f32_16x16x128_f8f6f4 v[62:65], v[130:137], v[66:73], v[62:65], v171, v170 op_sel_hi:[0,0,0]
	v_mfma_scale_f32_16x16x128_f8f6f4 v[58:61], v[138:145], v[66:73], v[58:61], v171, v170 op_sel_hi:[0,0,0]
	s_waitcnt lgkmcnt(4)
	v_mfma_scale_f32_16x16x128_f8f6f4 v[54:57], v[130:137], v[74:81], v[54:57], v171, v170 op_sel_hi:[0,0,0]
	v_mfma_scale_f32_16x16x128_f8f6f4 v[50:53], v[138:145], v[74:81], v[50:53], v171, v170 op_sel_hi:[0,0,0]
	s_waitcnt lgkmcnt(2)
	v_mfma_scale_f32_16x16x128_f8f6f4 v[204:207], v[130:137], v[82:89], v[46:49], v171, v170 op_sel_hi:[0,0,0]
	v_mfma_scale_f32_16x16x128_f8f6f4 v[212:215], v[138:145], v[82:89], v[42:45], v171, v170 op_sel_hi:[0,0,0]
	s_waitcnt lgkmcnt(0)
	v_mfma_scale_f32_16x16x128_f8f6f4 v[216:219], v[130:137], v[90:97], v[38:41], v171, v170 op_sel_hi:[0,0,0]
	v_mfma_scale_f32_16x16x128_f8f6f4 v[220:223], v[138:145], v[90:97], v[34:37], v171, v170 op_sel_hi:[0,0,0]
	s_setprio 0
	s_setprio 1
	v_mfma_scale_f32_16x16x128_f8f6f4 v[224:227], v[148:155], v[66:73], v[30:33], v171, v170 op_sel_hi:[0,0,0]
	v_mfma_scale_f32_16x16x128_f8f6f4 v[228:231], v[156:163], v[66:73], v[26:29], v171, v170 op_sel_hi:[0,0,0]
	v_mfma_scale_f32_16x16x128_f8f6f4 v[232:235], v[148:155], v[74:81], v[22:25], v171, v170 op_sel_hi:[0,0,0]
	v_mfma_scale_f32_16x16x128_f8f6f4 v[236:239], v[156:163], v[74:81], v[18:21], v171, v170 op_sel_hi:[0,0,0]
	v_mfma_scale_f32_16x16x128_f8f6f4 v[240:243], v[148:155], v[82:89], v[14:17], v171, v170 op_sel_hi:[0,0,0]
	v_mfma_scale_f32_16x16x128_f8f6f4 v[244:247], v[156:163], v[82:89], v[10:13], v171, v170 op_sel_hi:[0,0,0]
	v_mfma_scale_f32_16x16x128_f8f6f4 v[248:251], v[148:155], v[90:97], v[6:9], v171, v170 op_sel_hi:[0,0,0]
	v_mfma_scale_f32_16x16x128_f8f6f4 v[252:255], v[156:163], v[90:97], v[2:5], v171, v170 op_sel_hi:[0,0,0]
	s_setprio 0
	s_barrier
	s_nop 4
	ds_read_b128 v[2:5], v172
	ds_read_b128 v[6:9], v172 offset:1024
	ds_read_b128 v[10:13], v172 offset:2048
	ds_read_b128 v[14:17], v172 offset:3072
	ds_read_b128 v[130:133], v173
	ds_read_b128 v[134:137], v173 offset:1024
	ds_read_b128 v[138:141], v173 offset:2048
	ds_read_b128 v[142:145], v173 offset:3072
	s_mov_b32 m0, s39
	s_add_i32 s69, s30, 0x40000
	ds_read_b128 v[18:21], v169 offset:32768
	ds_read_b128 v[22:25], v169 offset:33792
	ds_read_b128 v[26:29], v169 offset:34816
	ds_read_b128 v[30:33], v169 offset:35840
	ds_read_b128 v[34:37], v169 offset:36864
	ds_read_b128 v[38:41], v169 offset:37888
	ds_read_b128 v[42:45], v169 offset:38912
	ds_read_b128 v[46:49], v169 offset:39936
	buffer_load_dwordx4 v1, s[12:15], s69 offen lds
	s_add_i32 s69, s30, 0x60000
	s_mov_b32 m0, s40
	s_nop 0
	buffer_load_dwordx4 v1, s[12:15], s69 offen lds
	s_waitcnt vmcnt(8)
	s_waitcnt lgkmcnt(0)
	s_barrier
	s_setprio 1
	s_waitcnt lgkmcnt(6)
	v_mfma_scale_f32_16x16x128_f8f6f4 v[126:129], v[2:9], v[18:25], v[126:129], v171, v170 op_sel_hi:[0,0,0]
	v_mfma_scale_f32_16x16x128_f8f6f4 v[122:125], v[10:17], v[18:25], v[122:125], v171, v170 op_sel_hi:[0,0,0]
	s_waitcnt lgkmcnt(4)
	v_mfma_scale_f32_16x16x128_f8f6f4 v[118:121], v[2:9], v[26:33], v[118:121], v171, v170 op_sel_hi:[0,0,0]
	v_mfma_scale_f32_16x16x128_f8f6f4 v[114:117], v[10:17], v[26:33], v[114:117], v171, v170 op_sel_hi:[0,0,0]
	s_waitcnt lgkmcnt(2)
	v_mfma_scale_f32_16x16x128_f8f6f4 v[110:113], v[2:9], v[34:41], v[110:113], v171, v170 op_sel_hi:[0,0,0]
	v_mfma_scale_f32_16x16x128_f8f6f4 v[106:109], v[10:17], v[34:41], v[106:109], v171, v170 op_sel_hi:[0,0,0]
	s_waitcnt lgkmcnt(0)
	v_mfma_scale_f32_16x16x128_f8f6f4 v[102:105], v[2:9], v[42:49], v[102:105], v171, v170 op_sel_hi:[0,0,0]
	v_mfma_scale_f32_16x16x128_f8f6f4 v[98:101], v[10:17], v[42:49], v[98:101], v171, v170 op_sel_hi:[0,0,0]
	s_setprio 0
	s_setprio 1
	v_mfma_scale_f32_16x16x128_f8f6f4 v[94:97], v[130:137], v[18:25], v[208:211], v171, v170 op_sel_hi:[0,0,0]
	v_mfma_scale_f32_16x16x128_f8f6f4 v[90:93], v[138:145], v[18:25], v[176:179], v171, v170 op_sel_hi:[0,0,0]
	v_mfma_scale_f32_16x16x128_f8f6f4 v[86:89], v[130:137], v[26:33], v[180:183], v171, v170 op_sel_hi:[0,0,0]
	v_mfma_scale_f32_16x16x128_f8f6f4 v[82:85], v[138:145], v[26:33], v[184:187], v171, v170 op_sel_hi:[0,0,0]
	v_mfma_scale_f32_16x16x128_f8f6f4 v[78:81], v[130:137], v[34:41], v[188:191], v171, v170 op_sel_hi:[0,0,0]
	v_mfma_scale_f32_16x16x128_f8f6f4 v[74:77], v[138:145], v[34:41], v[192:195], v171, v170 op_sel_hi:[0,0,0]
	v_mfma_scale_f32_16x16x128_f8f6f4 v[70:73], v[130:137], v[42:49], v[196:199], v171, v170 op_sel_hi:[0,0,0]
	v_mfma_scale_f32_16x16x128_f8f6f4 v[66:69], v[138:145], v[42:49], v[200:203], v171, v170 op_sel_hi:[0,0,0]
	s_setprio 0
	s_barrier
	s_mov_b32 m0, s42
	s_add_i32 s69, s68, 0x80
	ds_read_b128 v[18:21], v169 offset:49152
	ds_read_b128 v[22:25], v169 offset:50176
	ds_read_b128 v[148:151], v169 offset:51200
	ds_read_b128 v[152:155], v169 offset:52224
	ds_read_b128 v[156:159], v169 offset:53248
	ds_read_b128 v[160:163], v169 offset:54272
	ds_read_b128 v[176:179], v169 offset:55296
	ds_read_b128 v[180:183], v169 offset:56320
	buffer_load_dwordx4 v165, s[12:15], s69 offen lds
	s_add_i32 s69, s68, 0x20080
	s_mov_b32 m0, s43
	s_add_i32 s30, s30, 0x20080
	buffer_load_dwordx4 v165, s[12:15], s69 offen lds
	s_add_i32 s69, s68, 0x40080
	s_mov_b32 m0, s54
	s_add_i32 s68, s68, 0x60080
	buffer_load_dwordx4 v165, s[12:15], s69 offen lds
	s_mov_b32 m0, s55
	s_nop 0
	buffer_load_dwordx4 v165, s[12:15], s68 offen lds
	s_mov_b32 m0, s49
	s_nop 0
	buffer_load_dwordx4 v1, s[12:15], s31 offen lds
	s_mov_b32 m0, s53
	s_nop 0
	buffer_load_dwordx4 v1, s[12:15], s30 offen lds
	s_waitcnt vmcnt(8)
	s_waitcnt lgkmcnt(0)
	s_barrier
	s_setprio 1
	s_waitcnt lgkmcnt(6)
	v_mfma_scale_f32_16x16x128_f8f6f4 v[62:65], v[2:9], v[18:25], v[62:65], v171, v170 op_sel_hi:[0,0,0]
	v_mfma_scale_f32_16x16x128_f8f6f4 v[58:61], v[10:17], v[18:25], v[58:61], v171, v170 op_sel_hi:[0,0,0]
	s_waitcnt lgkmcnt(4)
	v_mfma_scale_f32_16x16x128_f8f6f4 v[54:57], v[2:9], v[148:155], v[54:57], v171, v170 op_sel_hi:[0,0,0]
	v_mfma_scale_f32_16x16x128_f8f6f4 v[50:53], v[10:17], v[148:155], v[50:53], v171, v170 op_sel_hi:[0,0,0]
	s_waitcnt lgkmcnt(2)
	v_mfma_scale_f32_16x16x128_f8f6f4 v[46:49], v[2:9], v[156:163], v[204:207], v171, v170 op_sel_hi:[0,0,0]
	v_mfma_scale_f32_16x16x128_f8f6f4 v[42:45], v[10:17], v[156:163], v[212:215], v171, v170 op_sel_hi:[0,0,0]
	s_waitcnt lgkmcnt(0)
	v_mfma_scale_f32_16x16x128_f8f6f4 v[38:41], v[2:9], v[176:183], v[216:219], v171, v170 op_sel_hi:[0,0,0]
	v_mfma_scale_f32_16x16x128_f8f6f4 v[34:37], v[10:17], v[176:183], v[220:223], v171, v170 op_sel_hi:[0,0,0]
	s_setprio 0
	s_setprio 1
	v_mfma_scale_f32_16x16x128_f8f6f4 v[30:33], v[130:137], v[18:25], v[224:227], v171, v170 op_sel_hi:[0,0,0]
	v_mfma_scale_f32_16x16x128_f8f6f4 v[26:29], v[138:145], v[18:25], v[228:231], v171, v170 op_sel_hi:[0,0,0]
	v_mfma_scale_f32_16x16x128_f8f6f4 v[22:25], v[130:137], v[148:155], v[232:235], v171, v170 op_sel_hi:[0,0,0]
	v_mfma_scale_f32_16x16x128_f8f6f4 v[18:21], v[138:145], v[148:155], v[236:239], v171, v170 op_sel_hi:[0,0,0]
	v_mfma_scale_f32_16x16x128_f8f6f4 v[14:17], v[130:137], v[156:163], v[240:243], v171, v170 op_sel_hi:[0,0,0]
	v_mfma_scale_f32_16x16x128_f8f6f4 v[10:13], v[138:145], v[156:163], v[244:247], v171, v170 op_sel_hi:[0,0,0]
	v_mfma_scale_f32_16x16x128_f8f6f4 v[6:9], v[130:137], v[176:183], v[248:251], v171, v170 op_sel_hi:[0,0,0]
	v_mfma_scale_f32_16x16x128_f8f6f4 v[2:5], v[138:145], v[176:183], v[252:255], v171, v170 op_sel_hi:[0,0,0]
	s_setprio 0
	s_add_i32 s11, s11, 2
	s_addk_i32 s8, 0x100
	s_addk_i32 s9, 0x100
	s_cmp_gt_u32 s11, 13
	s_cbranch_scc0 .Lkbar0
	s_barrier
	s_and_b64 vcc, exec, s[28:29]
	s_cbranch_vccz .LBB0_2429
	s_barrier
